# adds: longconv Z staging + output loop pipelined, s5c U staging, qkprep slot loop unrolled with prefetched row, V-transpose staging batched
# baseline (speedup 1.0000x reference)
; __device__ __forceinline__ void phase_longconv(const Params& P, unsigned char* smraw, int bid, int nb) {
;     ...
;             for (int e = tid; e < 128 * 32; e += NTHR) {
;                 const int row = e >> 5, d4 = (e & 31) * 4;
;                 const float4 v = *(const float4*)(Z + (size_t)c * NT + NCTX + row * 128 + d4);
;                 uint2 pk; pk.x = pack2(v.x, v.y); pk.y = pack2(v.z, v.w);
;                 *(uint2*)&Zs[row * HZ_STR + d4] = pk;
;             }
;             if (tid < HZ_STR / 2) ((unsigned*)&Zs[128 * HZ_STR])[tid] = 0u;
;             f32x16 acc[2][2];
; #pragma unroll
;             for (int i = 0; i < 2; ++i)
; #pragma unroll
;                 for (int j = 0; j < 2; ++j)
; #pragma unroll
;                     for (int q = 0; q < 16; ++q) acc[i][j][q] = 0.f;
;             const float* hf = HF + (size_t)c * 32768 + LSEQ;
;             float w0[3], w1[3], w2[3];
;     ...
;             HY_LOADW(0);
.LBB0_763:
	s_mov_b64 s[0:1], 0
	v_mov_b64_e32 v[4:5], v[164:165]
	v_mov_b32_e32 v2, v206
	v_mov_b32_e32 v6, v205
	s_barrier
	s_mov_b64 s[2:3], 0x2000
	global_load_dwordx4 v[220:223], v[4:5], off offset:-8
	v_lshl_add_u64 v[8:9], v[4:5], 0, s[2:3]
	global_load_dwordx4 v[224:227], v[8:9], off offset:-8
	v_lshl_add_u64 v[4:5], v[8:9], 0, s[2:3]
	global_load_dwordx4 v[228:231], v[4:5], off offset:-8
	v_lshl_add_u64 v[8:9], v[4:5], 0, s[2:3]
	global_load_dwordx4 v[232:235], v[8:9], off offset:-8
	v_lshl_add_u64 v[4:5], v[8:9], 0, s[2:3]
	global_load_dwordx4 v[236:239], v[4:5], off offset:-8
	v_lshl_add_u64 v[8:9], v[4:5], 0, s[2:3]
	global_load_dwordx4 v[240:243], v[8:9], off offset:-8
	v_lshl_add_u64 v[4:5], v[8:9], 0, s[2:3]
	global_load_dwordx4 v[244:247], v[4:5], off offset:-8
	v_lshl_add_u64 v[8:9], v[4:5], 0, s[2:3]
	global_load_dwordx4 v[248:251], v[8:9], off offset:-8
	s_waitcnt vmcnt(7)
	v_cvt_pk_bf16_f32 v220, v220, v221
	v_cvt_pk_bf16_f32 v221, v222, v223
	ds_write_b64 v2, v[220:221]
	s_waitcnt vmcnt(6)
	v_cvt_pk_bf16_f32 v224, v224, v225
	v_cvt_pk_bf16_f32 v225, v226, v227
	ds_write_b64 v2, v[224:225] offset:4352
	s_waitcnt vmcnt(5)
	v_cvt_pk_bf16_f32 v228, v228, v229
	v_cvt_pk_bf16_f32 v229, v230, v231
	ds_write_b64 v2, v[228:229] offset:8704
	s_waitcnt vmcnt(4)
	v_cvt_pk_bf16_f32 v232, v232, v233
	v_cvt_pk_bf16_f32 v233, v234, v235
	ds_write_b64 v2, v[232:233] offset:13056
	s_waitcnt vmcnt(3)
	v_cvt_pk_bf16_f32 v236, v236, v237
	v_cvt_pk_bf16_f32 v237, v238, v239
	ds_write_b64 v2, v[236:237] offset:17408
	s_waitcnt vmcnt(2)
	v_cvt_pk_bf16_f32 v240, v240, v241
	v_cvt_pk_bf16_f32 v241, v242, v243
	ds_write_b64 v2, v[240:241] offset:21760
	s_waitcnt vmcnt(1)
	v_cvt_pk_bf16_f32 v244, v244, v245
	v_cvt_pk_bf16_f32 v245, v246, v247
	ds_write_b64 v2, v[244:245] offset:26112
	s_waitcnt vmcnt(0)
	v_cvt_pk_bf16_f32 v248, v248, v249
	v_cvt_pk_bf16_f32 v249, v250, v251
	ds_write_b64 v2, v[248:249] offset:30464
	s_or_b64 exec, exec, s[0:1]
	s_and_saveexec_b64 s[0:1], s[6:7]
	ds_write_b32 v147, v3 offset:34832
	s_or_b64 exec, exec, s[0:1]
	s_ashr_i32 s67, s66, 31
	v_readlane_b32 s76, v252, 19
	s_lshl_b64 s[0:1], s[66:67], 17
	v_readlane_b32 s78, v252, 21
	v_readlane_b32 s79, v252, 22
	s_add_u32 s0, s78, s0
	s_addc_u32 s1, s79, s1
	s_add_u32 s68, s0, 0xe38000
	s_addc_u32 s69, s1, 0
	v_lshl_add_u64 v[4:5], v[148:149], 2, s[68:69]
	global_load_dwordx3 v[142:144], v[4:5], off
	v_mov_b32_e32 v215, 0
	v_mov_b32_e32 v214, 0
	v_readlane_b32 s77, v252, 20
	s_and_saveexec_b64 s[0:1], s[12:13]
	s_cbranch_execz .LBB0_769
	v_lshl_add_u64 v[4:5], v[150:151], 2, s[68:69]
	global_load_dword v214, v[4:5], off

; __device__ __forceinline__ bfr f2bf(float f) { return (bfr)(pack2(f, 0.f) & 0xffffu); }
; __device__ __forceinline__ void phase_longconv(const Params& P, unsigned char* smraw, int bid, int nb) {
;     ...
;                 for (int t = tid; t < LSEQ; t += NTHR) {
;                     const int b = t & 127, a_ = t >> 7;
;                     const int bt = b >> 5, rb = b & 31, at = a_ >> 5;
;                     const int hh = (rb >> 2) & 1, q = (rb & 3) + 4 * (rb >> 3);
;                     const int w = (bt >> 1) + 2 * (at >> 1);
;                     const int idx = (w * 64 + ((bt & 1) * 2 + (at & 1)) * 16 + q) * 64 + (a_ & 31) + 32 * hh;
;                     const float v = Red[idx] + Red[idx + 4 * 64 * 64];
;                     const int row = NCTX + t;
;                     const float x0 = X0[(size_t)c * NT + row];
;                     const float y = x0 * (v * nrm + Z[(size_t)c * NT + row] * sk);
;                     ATT[(size_t)row * 1024 + 512 + c] = f2bf(y);
;                 }
.LBB0_901:
	v_lshrrev_b32_e32 v13, 6, v8
	v_lshrrev_b32_e32 v11, 1, v8
	v_lshrrev_b32_e32 v12, 6, v9
	v_and_b32_e32 v13, 0x80, v13
	v_lshrrev_b32_e32 v15, 8, v8
	v_and_b32_e32 v17, 0x60, v8
	v_lshrrev_b32_e32 v2, 1, v9
	v_and_b32_e32 v11, 12, v11
	v_and_b32_e32 v12, 0x80, v12
	v_lshrrev_b32_e32 v14, 8, v9
	v_and_b32_e32 v15, 16, v15
	v_and_b32_e32 v16, 0x60, v9
	v_or_b32_e32 v13, v13, v17
	v_and_b32_e32 v2, 12, v2
	v_or_b32_e32 v11, v146, v11
	v_and_b32_e32 v14, 16, v14
	v_or_b32_e32 v12, v12, v16
	v_or_b32_e32 v13, v13, v15
	v_or_b32_e32 v2, v145, v2
	v_or_b32_e32 v12, v12, v14
	v_or_b32_e32 v11, v13, v11
	v_lshlrev_b32_e32 v13, 3, v8
	v_or_b32_e32 v2, v12, v2
	v_lshlrev_b32_e32 v12, 3, v9
	v_and_b32_e32 v13, 32, v13
	v_lshrrev_b32_e32 v14, 5, v8
	v_and_b32_e32 v12, 32, v12
	v_lshl_add_u32 v11, v11, 8, 0
	v_and_b32_e32 v14, 0x7c, v14
	v_lshrrev_b32_e32 v15, 5, v9
	v_lshlrev_b32_e32 v13, 2, v13
	v_lshl_add_u32 v2, v2, 8, 0
	v_and_b32_e32 v15, 0x7c, v15
	v_add3_u32 v11, v11, v14, v13
	v_lshlrev_b32_e32 v12, 2, v12
	v_add3_u32 v2, v2, v15, v12
	ds_read_b32 v12, v11 offset:16
	ds_read_b32 v13, v2 offset:16
	v_add_u32_e32 v11, 0x10010, v11
	v_add_u32_e32 v2, 0x10010, v2
	ds_read_b32 v14, v11
	ds_read_b32 v15, v2
	v_add_u32_e32 v2, 0x100, v8
	v_lshl_add_u64 v[18:19], s[0:1], 0, v[2:3]
	v_lshlrev_b64 v[18:19], 2, v[18:19]
	v_lshl_add_u64 v[20:21], s[60:61], 0, v[18:19]
	s_waitcnt lgkmcnt(0)
	v_pk_add_f32 v[224:225], v[12:13], v[14:15]
	v_add_u32_e32 v14, 0x100, v9
	v_mov_b32_e32 v15, v3
	v_lshl_add_u64 v[16:17], s[2:3], 0, v[14:15]
	v_lshlrev_b64 v[16:17], 2, v[16:17]
	v_lshl_add_u64 v[18:19], s[58:59], 0, v[18:19]
	v_lshl_add_u64 v[22:23], s[60:61], 0, v[16:17]
	global_load_dword v220, v[20:21], off
	s_nop 0
	global_load_dword v221, v[22:23], off
	v_lshl_add_u64 v[16:17], s[58:59], 0, v[16:17]
	global_load_dword v222, v[18:19], off
	s_nop 0
	global_load_dword v223, v[16:17], off
	v_add_u32_e32 v9, 0x400, v9
	v_add_u32_e32 v8, 0x400, v8
	v_lshrrev_b32_e32 v13, 6, v8
	v_lshrrev_b32_e32 v11, 1, v8
	v_lshrrev_b32_e32 v12, 6, v9
	v_and_b32_e32 v13, 0x80, v13
	v_lshrrev_b32_e32 v15, 8, v8
	v_and_b32_e32 v17, 0x60, v8
	v_lshrrev_b32_e32 v2, 1, v9
	v_and_b32_e32 v11, 12, v11
	v_and_b32_e32 v12, 0x80, v12
	v_lshrrev_b32_e32 v14, 8, v9
	v_and_b32_e32 v15, 16, v15
	v_and_b32_e32 v16, 0x60, v9
	v_or_b32_e32 v13, v13, v17
	v_and_b32_e32 v2, 12, v2
	v_or_b32_e32 v11, v146, v11
	v_and_b32_e32 v14, 16, v14
	v_or_b32_e32 v12, v12, v16
	v_or_b32_e32 v13, v13, v15
	v_or_b32_e32 v2, v145, v2
	v_or_b32_e32 v12, v12, v14
	v_or_b32_e32 v11, v13, v11
	v_lshlrev_b32_e32 v13, 3, v8
	v_or_b32_e32 v2, v12, v2
	v_lshlrev_b32_e32 v12, 3, v9
	v_and_b32_e32 v13, 32, v13
	v_lshrrev_b32_e32 v14, 5, v8
	v_and_b32_e32 v12, 32, v12
	v_lshl_add_u32 v11, v11, 8, 0
	v_and_b32_e32 v14, 0x7c, v14
	v_lshrrev_b32_e32 v15, 5, v9
	v_lshlrev_b32_e32 v13, 2, v13
	v_lshl_add_u32 v2, v2, 8, 0
	v_and_b32_e32 v15, 0x7c, v15
	v_add3_u32 v11, v11, v14, v13
	v_lshlrev_b32_e32 v12, 2, v12
	v_add3_u32 v2, v2, v15, v12
	ds_read_b32 v12, v11 offset:16
	ds_read_b32 v13, v2 offset:16
	v_add_u32_e32 v11, 0x10010, v11
	v_add_u32_e32 v2, 0x10010, v2
	ds_read_b32 v14, v11
	ds_read_b32 v15, v2
	v_add_u32_e32 v2, 0x100, v8
	v_lshl_add_u64 v[18:19], s[0:1], 0, v[2:3]
	v_lshlrev_b64 v[18:19], 2, v[18:19]
	v_lshl_add_u64 v[20:21], s[60:61], 0, v[18:19]
	s_waitcnt lgkmcnt(0)
	v_pk_add_f32 v[230:231], v[12:13], v[14:15]
	v_add_u32_e32 v14, 0x100, v9
	v_mov_b32_e32 v15, v3
	v_lshl_add_u64 v[16:17], s[2:3], 0, v[14:15]
	v_lshlrev_b64 v[16:17], 2, v[16:17]
	v_lshl_add_u64 v[18:19], s[58:59], 0, v[18:19]
	v_lshl_add_u64 v[22:23], s[60:61], 0, v[16:17]
	global_load_dword v226, v[20:21], off
	s_nop 0
	global_load_dword v227, v[22:23], off
	v_lshl_add_u64 v[16:17], s[58:59], 0, v[16:17]
	global_load_dword v228, v[18:19], off
	s_nop 0
	global_load_dword v229, v[16:17], off
	v_add_u32_e32 v9, 0x400, v9
	v_add_u32_e32 v8, 0x400, v8
	v_lshrrev_b32_e32 v13, 6, v8
	v_lshrrev_b32_e32 v11, 1, v8
	v_lshrrev_b32_e32 v12, 6, v9
	v_and_b32_e32 v13, 0x80, v13
	v_lshrrev_b32_e32 v15, 8, v8
	v_and_b32_e32 v17, 0x60, v8
	v_lshrrev_b32_e32 v2, 1, v9
	v_and_b32_e32 v11, 12, v11
	v_and_b32_e32 v12, 0x80, v12
	v_lshrrev_b32_e32 v14, 8, v9
	v_and_b32_e32 v15, 16, v15
	v_and_b32_e32 v16, 0x60, v9
	v_or_b32_e32 v13, v13, v17
	v_and_b32_e32 v2, 12, v2
	v_or_b32_e32 v11, v146, v11
	v_and_b32_e32 v14, 16, v14
	v_or_b32_e32 v12, v12, v16
	v_or_b32_e32 v13, v13, v15
	v_or_b32_e32 v2, v145, v2
	v_or_b32_e32 v12, v12, v14
	v_or_b32_e32 v11, v13, v11
	v_lshlrev_b32_e32 v13, 3, v8
	v_or_b32_e32 v2, v12, v2
	v_lshlrev_b32_e32 v12, 3, v9
	v_and_b32_e32 v13, 32, v13
	v_lshrrev_b32_e32 v14, 5, v8
	v_and_b32_e32 v12, 32, v12
	v_lshl_add_u32 v11, v11, 8, 0
	v_and_b32_e32 v14, 0x7c, v14
	v_lshrrev_b32_e32 v15, 5, v9
	v_lshlrev_b32_e32 v13, 2, v13
	v_lshl_add_u32 v2, v2, 8, 0
	v_and_b32_e32 v15, 0x7c, v15
	v_add3_u32 v11, v11, v14, v13
	v_lshlrev_b32_e32 v12, 2, v12
	v_add3_u32 v2, v2, v15, v12
	ds_read_b32 v12, v11 offset:16
	ds_read_b32 v13, v2 offset:16
	v_add_u32_e32 v11, 0x10010, v11
	v_add_u32_e32 v2, 0x10010, v2
	ds_read_b32 v14, v11
	ds_read_b32 v15, v2
	v_add_u32_e32 v2, 0x100, v8
	v_lshl_add_u64 v[18:19], s[0:1], 0, v[2:3]
	v_lshlrev_b64 v[18:19], 2, v[18:19]
	v_lshl_add_u64 v[20:21], s[60:61], 0, v[18:19]
	s_waitcnt lgkmcnt(0)
; __device__ __forceinline__ bfr f2bf(float f) { return (bfr)(pack2(f, 0.f) & 0xffffu); }
; __device__ __forceinline__ void phase_longconv(const Params& P, unsigned char* smraw, int bid, int nb) {
;     ...
;                 for (int t = tid; t < LSEQ; t += NTHR) {
;                     const int b = t & 127, a_ = t >> 7;
;                     const int bt = b >> 5, rb = b & 31, at = a_ >> 5;
;                     const int hh = (rb >> 2) & 1, q = (rb & 3) + 4 * (rb >> 3);
;                     const int w = (bt >> 1) + 2 * (at >> 1);
;                     const int idx = (w * 64 + ((bt & 1) * 2 + (at & 1)) * 16 + q) * 64 + (a_ & 31) + 32 * hh;
;                     const float v = Red[idx] + Red[idx + 4 * 64 * 64];
;                     const int row = NCTX + t;
;                     const float x0 = X0[(size_t)c * NT + row];
;                     const float y = x0 * (v * nrm + Z[(size_t)c * NT + row] * sk);
;                     ATT[(size_t)row * 1024 + 512 + c] = f2bf(y);
;                 }
	v_pk_add_f32 v[236:237], v[12:13], v[14:15]
	v_add_u32_e32 v14, 0x100, v9
	v_mov_b32_e32 v15, v3
	v_lshl_add_u64 v[16:17], s[2:3], 0, v[14:15]
	v_lshlrev_b64 v[16:17], 2, v[16:17]
	v_lshl_add_u64 v[18:19], s[58:59], 0, v[18:19]
	v_lshl_add_u64 v[22:23], s[60:61], 0, v[16:17]
	global_load_dword v232, v[20:21], off
	s_nop 0
	global_load_dword v233, v[22:23], off
	v_lshl_add_u64 v[16:17], s[58:59], 0, v[16:17]
	global_load_dword v234, v[18:19], off
	s_nop 0
	global_load_dword v235, v[16:17], off
	v_add_u32_e32 v9, 0x400, v9
	v_add_u32_e32 v8, 0x400, v8
	v_lshrrev_b32_e32 v13, 6, v8
	v_lshrrev_b32_e32 v11, 1, v8
	v_lshrrev_b32_e32 v12, 6, v9
	v_and_b32_e32 v13, 0x80, v13
	v_lshrrev_b32_e32 v15, 8, v8
	v_and_b32_e32 v17, 0x60, v8
	v_lshrrev_b32_e32 v2, 1, v9
	v_and_b32_e32 v11, 12, v11
	v_and_b32_e32 v12, 0x80, v12
	v_lshrrev_b32_e32 v14, 8, v9
	v_and_b32_e32 v15, 16, v15
	v_and_b32_e32 v16, 0x60, v9
	v_or_b32_e32 v13, v13, v17
	v_and_b32_e32 v2, 12, v2
	v_or_b32_e32 v11, v146, v11
	v_and_b32_e32 v14, 16, v14
	v_or_b32_e32 v12, v12, v16
	v_or_b32_e32 v13, v13, v15
	v_or_b32_e32 v2, v145, v2
	v_or_b32_e32 v12, v12, v14
	v_or_b32_e32 v11, v13, v11
	v_lshlrev_b32_e32 v13, 3, v8
	v_or_b32_e32 v2, v12, v2
	v_lshlrev_b32_e32 v12, 3, v9
	v_and_b32_e32 v13, 32, v13
	v_lshrrev_b32_e32 v14, 5, v8
	v_and_b32_e32 v12, 32, v12
	v_lshl_add_u32 v11, v11, 8, 0
	v_and_b32_e32 v14, 0x7c, v14
	v_lshrrev_b32_e32 v15, 5, v9
	v_lshlrev_b32_e32 v13, 2, v13
	v_lshl_add_u32 v2, v2, 8, 0
	v_and_b32_e32 v15, 0x7c, v15
	v_add3_u32 v11, v11, v14, v13
	v_lshlrev_b32_e32 v12, 2, v12
	v_add3_u32 v2, v2, v15, v12
	ds_read_b32 v12, v11 offset:16
	ds_read_b32 v13, v2 offset:16
	v_add_u32_e32 v11, 0x10010, v11
	v_add_u32_e32 v2, 0x10010, v2
	ds_read_b32 v14, v11
	ds_read_b32 v15, v2
	v_add_u32_e32 v2, 0x100, v8
	v_lshl_add_u64 v[18:19], s[0:1], 0, v[2:3]
	v_lshlrev_b64 v[18:19], 2, v[18:19]
	v_lshl_add_u64 v[20:21], s[60:61], 0, v[18:19]
	s_waitcnt lgkmcnt(0)
	v_pk_add_f32 v[242:243], v[12:13], v[14:15]
	v_add_u32_e32 v14, 0x100, v9
	v_mov_b32_e32 v15, v3
	v_lshl_add_u64 v[16:17], s[2:3], 0, v[14:15]
	v_lshlrev_b64 v[16:17], 2, v[16:17]
	v_lshl_add_u64 v[18:19], s[58:59], 0, v[18:19]
	v_lshl_add_u64 v[22:23], s[60:61], 0, v[16:17]
	global_load_dword v238, v[20:21], off
	s_nop 0
	global_load_dword v239, v[22:23], off
	v_lshl_add_u64 v[16:17], s[58:59], 0, v[16:17]
	global_load_dword v240, v[18:19], off
	s_nop 0
	global_load_dword v241, v[16:17], off
	v_add_u32_e32 v9, 0x400, v9
	v_add_u32_e32 v8, 0x400, v8
	s_waitcnt vmcnt(12)
	v_pk_mul_f32 v[16:17], v[6:7], v[222:223]
	s_nop 0
	v_pk_fma_f32 v[12:13], v[4:5], v[224:225], v[16:17]
	s_nop 0
	v_pk_mul_f32 v[12:13], v[220:221], v[12:13]
	s_nop 0
	v_cvt_pk_bf16_f32 v11, v12, v13
	v_add_u32_e32 v14, 0x100, v1
	v_mov_b32_e32 v15, v3
	v_add_u32_e32 v2, 0x100, v0
	v_lshlrev_b64 v[12:13], 11, v[14:15]
	v_lshlrev_b64 v[14:15], 11, v[2:3]
	v_lshl_add_u64 v[14:15], s[4:5], 0, v[14:15]
	v_lshl_add_u64 v[12:13], s[4:5], 0, v[12:13]
	global_store_short v[14:15], v11, off offset:1024
	global_store_short_d16_hi v[12:13], v11, off offset:1024
	v_lshrrev_b32_e32 v13, 6, v8
	v_lshrrev_b32_e32 v11, 1, v8
	v_lshrrev_b32_e32 v12, 6, v9
	v_and_b32_e32 v13, 0x80, v13
	v_lshrrev_b32_e32 v15, 8, v8
	v_and_b32_e32 v17, 0x60, v8
	v_lshrrev_b32_e32 v2, 1, v9
	v_and_b32_e32 v11, 12, v11
	v_and_b32_e32 v12, 0x80, v12
	v_lshrrev_b32_e32 v14, 8, v9
	v_and_b32_e32 v15, 16, v15
	v_and_b32_e32 v16, 0x60, v9
	v_or_b32_e32 v13, v13, v17
	v_and_b32_e32 v2, 12, v2
	v_or_b32_e32 v11, v146, v11
	v_and_b32_e32 v14, 16, v14
	v_or_b32_e32 v12, v12, v16
	v_or_b32_e32 v13, v13, v15
	v_or_b32_e32 v2, v145, v2
	v_or_b32_e32 v12, v12, v14
	v_or_b32_e32 v11, v13, v11
	v_lshlrev_b32_e32 v13, 3, v8
	v_or_b32_e32 v2, v12, v2
	v_lshlrev_b32_e32 v12, 3, v9
	v_and_b32_e32 v13, 32, v13
	v_lshrrev_b32_e32 v14, 5, v8
	v_and_b32_e32 v12, 32, v12
	v_lshl_add_u32 v11, v11, 8, 0
	v_and_b32_e32 v14, 0x7c, v14
	v_lshrrev_b32_e32 v15, 5, v9
	v_lshlrev_b32_e32 v13, 2, v13
	v_lshl_add_u32 v2, v2, 8, 0
	v_and_b32_e32 v15, 0x7c, v15
	v_add3_u32 v11, v11, v14, v13
	v_lshlrev_b32_e32 v12, 2, v12
	v_add3_u32 v2, v2, v15, v12
	ds_read_b32 v12, v11 offset:16
	ds_read_b32 v13, v2 offset:16
	v_add_u32_e32 v11, 0x10010, v11
	v_add_u32_e32 v2, 0x10010, v2
	ds_read_b32 v14, v11
	ds_read_b32 v15, v2
	v_add_u32_e32 v2, 0x100, v8
	v_lshl_add_u64 v[18:19], s[0:1], 0, v[2:3]
	v_lshlrev_b64 v[18:19], 2, v[18:19]
	v_lshl_add_u64 v[20:21], s[60:61], 0, v[18:19]
	s_waitcnt lgkmcnt(0)
	v_pk_add_f32 v[224:225], v[12:13], v[14:15]
	v_add_u32_e32 v14, 0x100, v9
	v_mov_b32_e32 v15, v3
	v_lshl_add_u64 v[16:17], s[2:3], 0, v[14:15]
	v_lshlrev_b64 v[16:17], 2, v[16:17]
	v_lshl_add_u64 v[18:19], s[58:59], 0, v[18:19]
	v_lshl_add_u64 v[22:23], s[60:61], 0, v[16:17]
	global_load_dword v220, v[20:21], off
	s_nop 0
	global_load_dword v221, v[22:23], off
	v_lshl_add_u64 v[16:17], s[58:59], 0, v[16:17]
	global_load_dword v222, v[18:19], off
	s_nop 0
	global_load_dword v223, v[16:17], off
	v_add_u32_e32 v9, 0x400, v9
	v_add_u32_e32 v8, 0x400, v8
	s_waitcnt vmcnt(14)
; __device__ __forceinline__ bfr f2bf(float f) { return (bfr)(pack2(f, 0.f) & 0xffffu); }
; __device__ __forceinline__ void phase_longconv(const Params& P, unsigned char* smraw, int bid, int nb) {
;     ...
;                 for (int t = tid; t < LSEQ; t += NTHR) {
;                     const int b = t & 127, a_ = t >> 7;
;                     const int bt = b >> 5, rb = b & 31, at = a_ >> 5;
;                     const int hh = (rb >> 2) & 1, q = (rb & 3) + 4 * (rb >> 3);
;                     const int w = (bt >> 1) + 2 * (at >> 1);
;                     const int idx = (w * 64 + ((bt & 1) * 2 + (at & 1)) * 16 + q) * 64 + (a_ & 31) + 32 * hh;
;                     const float v = Red[idx] + Red[idx + 4 * 64 * 64];
;                     const int row = NCTX + t;
;                     const float x0 = X0[(size_t)c * NT + row];
;                     const float y = x0 * (v * nrm + Z[(size_t)c * NT + row] * sk);
;                     ATT[(size_t)row * 1024 + 512 + c] = f2bf(y);
;                 }
	v_pk_mul_f32 v[16:17], v[6:7], v[228:229]
	s_nop 0
	v_pk_fma_f32 v[12:13], v[4:5], v[230:231], v[16:17]
	s_nop 0
	v_pk_mul_f32 v[12:13], v[226:227], v[12:13]
	s_nop 0
	v_cvt_pk_bf16_f32 v11, v12, v13
	v_add_u32_e32 v14, 0x500, v1
	v_mov_b32_e32 v15, v3
	v_add_u32_e32 v2, 0x500, v0
	v_lshlrev_b64 v[12:13], 11, v[14:15]
	v_lshlrev_b64 v[14:15], 11, v[2:3]
	v_lshl_add_u64 v[14:15], s[4:5], 0, v[14:15]
	v_lshl_add_u64 v[12:13], s[4:5], 0, v[12:13]
	global_store_short v[14:15], v11, off offset:1024
	global_store_short_d16_hi v[12:13], v11, off offset:1024
	v_lshrrev_b32_e32 v13, 6, v8
	v_lshrrev_b32_e32 v11, 1, v8
	v_lshrrev_b32_e32 v12, 6, v9
	v_and_b32_e32 v13, 0x80, v13
	v_lshrrev_b32_e32 v15, 8, v8
	v_and_b32_e32 v17, 0x60, v8
	v_lshrrev_b32_e32 v2, 1, v9
	v_and_b32_e32 v11, 12, v11
	v_and_b32_e32 v12, 0x80, v12
	v_lshrrev_b32_e32 v14, 8, v9
	v_and_b32_e32 v15, 16, v15
	v_and_b32_e32 v16, 0x60, v9
	v_or_b32_e32 v13, v13, v17
	v_and_b32_e32 v2, 12, v2
	v_or_b32_e32 v11, v146, v11
	v_and_b32_e32 v14, 16, v14
	v_or_b32_e32 v12, v12, v16
	v_or_b32_e32 v13, v13, v15
	v_or_b32_e32 v2, v145, v2
	v_or_b32_e32 v12, v12, v14
	v_or_b32_e32 v11, v13, v11
	v_lshlrev_b32_e32 v13, 3, v8
	v_or_b32_e32 v2, v12, v2
	v_lshlrev_b32_e32 v12, 3, v9
	v_and_b32_e32 v13, 32, v13
	v_lshrrev_b32_e32 v14, 5, v8
	v_and_b32_e32 v12, 32, v12
	v_lshl_add_u32 v11, v11, 8, 0
	v_and_b32_e32 v14, 0x7c, v14
	v_lshrrev_b32_e32 v15, 5, v9
	v_lshlrev_b32_e32 v13, 2, v13
	v_lshl_add_u32 v2, v2, 8, 0
	v_and_b32_e32 v15, 0x7c, v15
	v_add3_u32 v11, v11, v14, v13
	v_lshlrev_b32_e32 v12, 2, v12
	v_add3_u32 v2, v2, v15, v12
	ds_read_b32 v12, v11 offset:16
	ds_read_b32 v13, v2 offset:16
	v_add_u32_e32 v11, 0x10010, v11
	v_add_u32_e32 v2, 0x10010, v2
	ds_read_b32 v14, v11
	ds_read_b32 v15, v2
	v_add_u32_e32 v2, 0x100, v8
	v_lshl_add_u64 v[18:19], s[0:1], 0, v[2:3]
	v_lshlrev_b64 v[18:19], 2, v[18:19]
	v_lshl_add_u64 v[20:21], s[60:61], 0, v[18:19]
	s_waitcnt lgkmcnt(0)
	v_pk_add_f32 v[230:231], v[12:13], v[14:15]
	v_add_u32_e32 v14, 0x100, v9
	v_mov_b32_e32 v15, v3
	v_lshl_add_u64 v[16:17], s[2:3], 0, v[14:15]
	v_lshlrev_b64 v[16:17], 2, v[16:17]
	v_lshl_add_u64 v[18:19], s[58:59], 0, v[18:19]
	v_lshl_add_u64 v[22:23], s[60:61], 0, v[16:17]
	global_load_dword v226, v[20:21], off
	s_nop 0
	global_load_dword v227, v[22:23], off
	v_lshl_add_u64 v[16:17], s[58:59], 0, v[16:17]
	global_load_dword v228, v[18:19], off
	s_nop 0
	global_load_dword v229, v[16:17], off
	v_add_u32_e32 v9, 0x400, v9
	v_add_u32_e32 v8, 0x400, v8
	s_waitcnt vmcnt(16)
	v_pk_mul_f32 v[16:17], v[6:7], v[234:235]
	s_nop 0
	v_pk_fma_f32 v[12:13], v[4:5], v[236:237], v[16:17]
	s_nop 0
	v_pk_mul_f32 v[12:13], v[232:233], v[12:13]
	s_nop 0
	v_cvt_pk_bf16_f32 v11, v12, v13
	v_add_u32_e32 v14, 0x900, v1
	v_mov_b32_e32 v15, v3
	v_add_u32_e32 v2, 0x900, v0
	v_lshlrev_b64 v[12:13], 11, v[14:15]
	v_lshlrev_b64 v[14:15], 11, v[2:3]
	v_lshl_add_u64 v[14:15], s[4:5], 0, v[14:15]
	v_lshl_add_u64 v[12:13], s[4:5], 0, v[12:13]
	global_store_short v[14:15], v11, off offset:1024
	global_store_short_d16_hi v[12:13], v11, off offset:1024
	v_lshrrev_b32_e32 v13, 6, v8
	v_lshrrev_b32_e32 v11, 1, v8
	v_lshrrev_b32_e32 v12, 6, v9
	v_and_b32_e32 v13, 0x80, v13
	v_lshrrev_b32_e32 v15, 8, v8
	v_and_b32_e32 v17, 0x60, v8
	v_lshrrev_b32_e32 v2, 1, v9
	v_and_b32_e32 v11, 12, v11
	v_and_b32_e32 v12, 0x80, v12
	v_lshrrev_b32_e32 v14, 8, v9
	v_and_b32_e32 v15, 16, v15
	v_and_b32_e32 v16, 0x60, v9
	v_or_b32_e32 v13, v13, v17
	v_and_b32_e32 v2, 12, v2
	v_or_b32_e32 v11, v146, v11
	v_and_b32_e32 v14, 16, v14
	v_or_b32_e32 v12, v12, v16
	v_or_b32_e32 v13, v13, v15
	v_or_b32_e32 v2, v145, v2
	v_or_b32_e32 v12, v12, v14
	v_or_b32_e32 v11, v13, v11
	v_lshlrev_b32_e32 v13, 3, v8
	v_or_b32_e32 v2, v12, v2
	v_lshlrev_b32_e32 v12, 3, v9
	v_and_b32_e32 v13, 32, v13
	v_lshrrev_b32_e32 v14, 5, v8
	v_and_b32_e32 v12, 32, v12
	v_lshl_add_u32 v11, v11, 8, 0
	v_and_b32_e32 v14, 0x7c, v14
	v_lshrrev_b32_e32 v15, 5, v9
	v_lshlrev_b32_e32 v13, 2, v13
	v_lshl_add_u32 v2, v2, 8, 0
	v_and_b32_e32 v15, 0x7c, v15
	v_add3_u32 v11, v11, v14, v13
	v_lshlrev_b32_e32 v12, 2, v12
	v_add3_u32 v2, v2, v15, v12
	ds_read_b32 v12, v11 offset:16
	ds_read_b32 v13, v2 offset:16
	v_add_u32_e32 v11, 0x10010, v11
	v_add_u32_e32 v2, 0x10010, v2
	ds_read_b32 v14, v11
	ds_read_b32 v15, v2
	v_add_u32_e32 v2, 0x100, v8
	v_lshl_add_u64 v[18:19], s[0:1], 0, v[2:3]
	v_lshlrev_b64 v[18:19], 2, v[18:19]
	v_lshl_add_u64 v[20:21], s[60:61], 0, v[18:19]
	s_waitcnt lgkmcnt(0)
	v_pk_add_f32 v[236:237], v[12:13], v[14:15]
	v_add_u32_e32 v14, 0x100, v9
	v_mov_b32_e32 v15, v3
	v_lshl_add_u64 v[16:17], s[2:3], 0, v[14:15]
	v_lshlrev_b64 v[16:17], 2, v[16:17]
	v_lshl_add_u64 v[18:19], s[58:59], 0, v[18:19]
	v_lshl_add_u64 v[22:23], s[60:61], 0, v[16:17]
	global_load_dword v232, v[20:21], off
	s_nop 0
	global_load_dword v233, v[22:23], off
	v_lshl_add_u64 v[16:17], s[58:59], 0, v[16:17]
	global_load_dword v234, v[18:19], off
	s_nop 0
	global_load_dword v235, v[16:17], off
	v_add_u32_e32 v9, 0x400, v9
	v_add_u32_e32 v8, 0x400, v8
	s_waitcnt vmcnt(18)
; __device__ __forceinline__ bfr f2bf(float f) { return (bfr)(pack2(f, 0.f) & 0xffffu); }
; __device__ __forceinline__ void phase_longconv(const Params& P, unsigned char* smraw, int bid, int nb) {
;     ...
;                 for (int t = tid; t < LSEQ; t += NTHR) {
;                     const int b = t & 127, a_ = t >> 7;
;                     const int bt = b >> 5, rb = b & 31, at = a_ >> 5;
;                     const int hh = (rb >> 2) & 1, q = (rb & 3) + 4 * (rb >> 3);
;                     const int w = (bt >> 1) + 2 * (at >> 1);
;                     const int idx = (w * 64 + ((bt & 1) * 2 + (at & 1)) * 16 + q) * 64 + (a_ & 31) + 32 * hh;
;                     const float v = Red[idx] + Red[idx + 4 * 64 * 64];
;                     const int row = NCTX + t;
;                     const float x0 = X0[(size_t)c * NT + row];
;                     const float y = x0 * (v * nrm + Z[(size_t)c * NT + row] * sk);
;                     ATT[(size_t)row * 1024 + 512 + c] = f2bf(y);
;                 }
	v_pk_mul_f32 v[16:17], v[6:7], v[240:241]
	s_nop 0
	v_pk_fma_f32 v[12:13], v[4:5], v[242:243], v[16:17]
	s_nop 0
	v_pk_mul_f32 v[12:13], v[238:239], v[12:13]
	s_nop 0
	v_cvt_pk_bf16_f32 v11, v12, v13
	v_add_u32_e32 v14, 0xd00, v1
	v_mov_b32_e32 v15, v3
	v_add_u32_e32 v2, 0xd00, v0
	v_lshlrev_b64 v[12:13], 11, v[14:15]
	v_lshlrev_b64 v[14:15], 11, v[2:3]
	v_lshl_add_u64 v[14:15], s[4:5], 0, v[14:15]
	v_lshl_add_u64 v[12:13], s[4:5], 0, v[12:13]
	global_store_short v[14:15], v11, off offset:1024
	global_store_short_d16_hi v[12:13], v11, off offset:1024
	v_lshrrev_b32_e32 v13, 6, v8
	v_lshrrev_b32_e32 v11, 1, v8
	v_lshrrev_b32_e32 v12, 6, v9
	v_and_b32_e32 v13, 0x80, v13
	v_lshrrev_b32_e32 v15, 8, v8
	v_and_b32_e32 v17, 0x60, v8
	v_lshrrev_b32_e32 v2, 1, v9
	v_and_b32_e32 v11, 12, v11
	v_and_b32_e32 v12, 0x80, v12
	v_lshrrev_b32_e32 v14, 8, v9
	v_and_b32_e32 v15, 16, v15
	v_and_b32_e32 v16, 0x60, v9
	v_or_b32_e32 v13, v13, v17
	v_and_b32_e32 v2, 12, v2
	v_or_b32_e32 v11, v146, v11
	v_and_b32_e32 v14, 16, v14
	v_or_b32_e32 v12, v12, v16
	v_or_b32_e32 v13, v13, v15
	v_or_b32_e32 v2, v145, v2
	v_or_b32_e32 v12, v12, v14
	v_or_b32_e32 v11, v13, v11
	v_lshlrev_b32_e32 v13, 3, v8
	v_or_b32_e32 v2, v12, v2
	v_lshlrev_b32_e32 v12, 3, v9
	v_and_b32_e32 v13, 32, v13
	v_lshrrev_b32_e32 v14, 5, v8
	v_and_b32_e32 v12, 32, v12
	v_lshl_add_u32 v11, v11, 8, 0
	v_and_b32_e32 v14, 0x7c, v14
	v_lshrrev_b32_e32 v15, 5, v9
	v_lshlrev_b32_e32 v13, 2, v13
	v_lshl_add_u32 v2, v2, 8, 0
	v_and_b32_e32 v15, 0x7c, v15
	v_add3_u32 v11, v11, v14, v13
	v_lshlrev_b32_e32 v12, 2, v12
	v_add3_u32 v2, v2, v15, v12
	ds_read_b32 v12, v11 offset:16
	ds_read_b32 v13, v2 offset:16
	v_add_u32_e32 v11, 0x10010, v11
	v_add_u32_e32 v2, 0x10010, v2
	ds_read_b32 v14, v11
	ds_read_b32 v15, v2
	v_add_u32_e32 v2, 0x100, v8
	v_lshl_add_u64 v[18:19], s[0:1], 0, v[2:3]
	v_lshlrev_b64 v[18:19], 2, v[18:19]
	v_lshl_add_u64 v[20:21], s[60:61], 0, v[18:19]
	s_waitcnt lgkmcnt(0)
	v_pk_add_f32 v[242:243], v[12:13], v[14:15]
	v_add_u32_e32 v14, 0x100, v9
	v_mov_b32_e32 v15, v3
	v_lshl_add_u64 v[16:17], s[2:3], 0, v[14:15]
	v_lshlrev_b64 v[16:17], 2, v[16:17]
	v_lshl_add_u64 v[18:19], s[58:59], 0, v[18:19]
	v_lshl_add_u64 v[22:23], s[60:61], 0, v[16:17]
	global_load_dword v238, v[20:21], off
	s_nop 0
	global_load_dword v239, v[22:23], off
	v_lshl_add_u64 v[16:17], s[58:59], 0, v[16:17]
	global_load_dword v240, v[18:19], off
	s_nop 0
	global_load_dword v241, v[16:17], off
	v_add_u32_e32 v9, 0x400, v9
	v_add_u32_e32 v8, 0x400, v8
	s_waitcnt vmcnt(18)
	v_pk_mul_f32 v[16:17], v[6:7], v[222:223]
	s_nop 0
	v_pk_fma_f32 v[12:13], v[4:5], v[224:225], v[16:17]
	s_nop 0
	v_pk_mul_f32 v[12:13], v[220:221], v[12:13]
	s_nop 0
	v_cvt_pk_bf16_f32 v11, v12, v13
	v_add_u32_e32 v14, 0x1100, v1
	v_mov_b32_e32 v15, v3
	v_add_u32_e32 v2, 0x1100, v0
	v_lshlrev_b64 v[12:13], 11, v[14:15]
	v_lshlrev_b64 v[14:15], 11, v[2:3]
	v_lshl_add_u64 v[14:15], s[4:5], 0, v[14:15]
	v_lshl_add_u64 v[12:13], s[4:5], 0, v[12:13]
	global_store_short v[14:15], v11, off offset:1024
	global_store_short_d16_hi v[12:13], v11, off offset:1024
	v_lshrrev_b32_e32 v13, 6, v8
	v_lshrrev_b32_e32 v11, 1, v8
	v_lshrrev_b32_e32 v12, 6, v9
	v_and_b32_e32 v13, 0x80, v13
	v_lshrrev_b32_e32 v15, 8, v8
	v_and_b32_e32 v17, 0x60, v8
	v_lshrrev_b32_e32 v2, 1, v9
	v_and_b32_e32 v11, 12, v11
	v_and_b32_e32 v12, 0x80, v12
	v_lshrrev_b32_e32 v14, 8, v9
	v_and_b32_e32 v15, 16, v15
	v_and_b32_e32 v16, 0x60, v9
	v_or_b32_e32 v13, v13, v17
	v_and_b32_e32 v2, 12, v2
	v_or_b32_e32 v11, v146, v11
	v_and_b32_e32 v14, 16, v14
	v_or_b32_e32 v12, v12, v16
	v_or_b32_e32 v13, v13, v15
	v_or_b32_e32 v2, v145, v2
	v_or_b32_e32 v12, v12, v14
	v_or_b32_e32 v11, v13, v11
	v_lshlrev_b32_e32 v13, 3, v8
	v_or_b32_e32 v2, v12, v2
	v_lshlrev_b32_e32 v12, 3, v9
	v_and_b32_e32 v13, 32, v13
	v_lshrrev_b32_e32 v14, 5, v8
	v_and_b32_e32 v12, 32, v12
	v_lshl_add_u32 v11, v11, 8, 0
	v_and_b32_e32 v14, 0x7c, v14
	v_lshrrev_b32_e32 v15, 5, v9
	v_lshlrev_b32_e32 v13, 2, v13
	v_lshl_add_u32 v2, v2, 8, 0
	v_and_b32_e32 v15, 0x7c, v15
	v_add3_u32 v11, v11, v14, v13
	v_lshlrev_b32_e32 v12, 2, v12
	v_add3_u32 v2, v2, v15, v12
	ds_read_b32 v12, v11 offset:16
	ds_read_b32 v13, v2 offset:16
	v_add_u32_e32 v11, 0x10010, v11
	v_add_u32_e32 v2, 0x10010, v2
	ds_read_b32 v14, v11
	ds_read_b32 v15, v2
	v_add_u32_e32 v2, 0x100, v8
	v_lshl_add_u64 v[18:19], s[0:1], 0, v[2:3]
	v_lshlrev_b64 v[18:19], 2, v[18:19]
	v_lshl_add_u64 v[20:21], s[60:61], 0, v[18:19]
	s_waitcnt lgkmcnt(0)
	v_pk_add_f32 v[224:225], v[12:13], v[14:15]
	v_add_u32_e32 v14, 0x100, v9
	v_mov_b32_e32 v15, v3
	v_lshl_add_u64 v[16:17], s[2:3], 0, v[14:15]
	v_lshlrev_b64 v[16:17], 2, v[16:17]
	v_lshl_add_u64 v[18:19], s[58:59], 0, v[18:19]
	v_lshl_add_u64 v[22:23], s[60:61], 0, v[16:17]
	global_load_dword v220, v[20:21], off
	s_nop 0
	global_load_dword v221, v[22:23], off
	v_lshl_add_u64 v[16:17], s[58:59], 0, v[16:17]
	global_load_dword v222, v[18:19], off
	s_nop 0
	global_load_dword v223, v[16:17], off
	v_add_u32_e32 v9, 0x400, v9
	v_add_u32_e32 v8, 0x400, v8
	s_waitcnt vmcnt(18)
; __device__ __forceinline__ bfr f2bf(float f) { return (bfr)(pack2(f, 0.f) & 0xffffu); }
; __device__ __forceinline__ void phase_longconv(const Params& P, unsigned char* smraw, int bid, int nb) {
;     ...
;                 for (int t = tid; t < LSEQ; t += NTHR) {
;                     const int b = t & 127, a_ = t >> 7;
;                     const int bt = b >> 5, rb = b & 31, at = a_ >> 5;
;                     const int hh = (rb >> 2) & 1, q = (rb & 3) + 4 * (rb >> 3);
;                     const int w = (bt >> 1) + 2 * (at >> 1);
;                     const int idx = (w * 64 + ((bt & 1) * 2 + (at & 1)) * 16 + q) * 64 + (a_ & 31) + 32 * hh;
;                     const float v = Red[idx] + Red[idx + 4 * 64 * 64];
;                     const int row = NCTX + t;
;                     const float x0 = X0[(size_t)c * NT + row];
;                     const float y = x0 * (v * nrm + Z[(size_t)c * NT + row] * sk);
;                     ATT[(size_t)row * 1024 + 512 + c] = f2bf(y);
;                 }
	v_pk_mul_f32 v[16:17], v[6:7], v[228:229]
	s_nop 0
	v_pk_fma_f32 v[12:13], v[4:5], v[230:231], v[16:17]
	s_nop 0
	v_pk_mul_f32 v[12:13], v[226:227], v[12:13]
	s_nop 0
	v_cvt_pk_bf16_f32 v11, v12, v13
	v_add_u32_e32 v14, 0x1500, v1
	v_mov_b32_e32 v15, v3
	v_add_u32_e32 v2, 0x1500, v0
	v_lshlrev_b64 v[12:13], 11, v[14:15]
	v_lshlrev_b64 v[14:15], 11, v[2:3]
	v_lshl_add_u64 v[14:15], s[4:5], 0, v[14:15]
	v_lshl_add_u64 v[12:13], s[4:5], 0, v[12:13]
	global_store_short v[14:15], v11, off offset:1024
	global_store_short_d16_hi v[12:13], v11, off offset:1024
	v_lshrrev_b32_e32 v13, 6, v8
	v_lshrrev_b32_e32 v11, 1, v8
	v_lshrrev_b32_e32 v12, 6, v9
	v_and_b32_e32 v13, 0x80, v13
	v_lshrrev_b32_e32 v15, 8, v8
	v_and_b32_e32 v17, 0x60, v8
	v_lshrrev_b32_e32 v2, 1, v9
	v_and_b32_e32 v11, 12, v11
	v_and_b32_e32 v12, 0x80, v12
	v_lshrrev_b32_e32 v14, 8, v9
	v_and_b32_e32 v15, 16, v15
	v_and_b32_e32 v16, 0x60, v9
	v_or_b32_e32 v13, v13, v17
	v_and_b32_e32 v2, 12, v2
	v_or_b32_e32 v11, v146, v11
	v_and_b32_e32 v14, 16, v14
	v_or_b32_e32 v12, v12, v16
	v_or_b32_e32 v13, v13, v15
	v_or_b32_e32 v2, v145, v2
	v_or_b32_e32 v12, v12, v14
	v_or_b32_e32 v11, v13, v11
	v_lshlrev_b32_e32 v13, 3, v8
	v_or_b32_e32 v2, v12, v2
	v_lshlrev_b32_e32 v12, 3, v9
	v_and_b32_e32 v13, 32, v13
	v_lshrrev_b32_e32 v14, 5, v8
	v_and_b32_e32 v12, 32, v12
	v_lshl_add_u32 v11, v11, 8, 0
	v_and_b32_e32 v14, 0x7c, v14
	v_lshrrev_b32_e32 v15, 5, v9
	v_lshlrev_b32_e32 v13, 2, v13
	v_lshl_add_u32 v2, v2, 8, 0
	v_and_b32_e32 v15, 0x7c, v15
	v_add3_u32 v11, v11, v14, v13
	v_lshlrev_b32_e32 v12, 2, v12
	v_add3_u32 v2, v2, v15, v12
	ds_read_b32 v12, v11 offset:16
	ds_read_b32 v13, v2 offset:16
	v_add_u32_e32 v11, 0x10010, v11
	v_add_u32_e32 v2, 0x10010, v2
	ds_read_b32 v14, v11
	ds_read_b32 v15, v2
	v_add_u32_e32 v2, 0x100, v8
	v_lshl_add_u64 v[18:19], s[0:1], 0, v[2:3]
	v_lshlrev_b64 v[18:19], 2, v[18:19]
	v_lshl_add_u64 v[20:21], s[60:61], 0, v[18:19]
	s_waitcnt lgkmcnt(0)
	v_pk_add_f32 v[230:231], v[12:13], v[14:15]
	v_add_u32_e32 v14, 0x100, v9
	v_mov_b32_e32 v15, v3
	v_lshl_add_u64 v[16:17], s[2:3], 0, v[14:15]
	v_lshlrev_b64 v[16:17], 2, v[16:17]
	v_lshl_add_u64 v[18:19], s[58:59], 0, v[18:19]
	v_lshl_add_u64 v[22:23], s[60:61], 0, v[16:17]
	global_load_dword v226, v[20:21], off
	s_nop 0
	global_load_dword v227, v[22:23], off
	v_lshl_add_u64 v[16:17], s[58:59], 0, v[16:17]
	global_load_dword v228, v[18:19], off
	s_nop 0
	global_load_dword v229, v[16:17], off
	v_add_u32_e32 v9, 0x400, v9
	v_add_u32_e32 v8, 0x400, v8
	s_waitcnt vmcnt(18)
	v_pk_mul_f32 v[16:17], v[6:7], v[234:235]
	s_nop 0
	v_pk_fma_f32 v[12:13], v[4:5], v[236:237], v[16:17]
	s_nop 0
	v_pk_mul_f32 v[12:13], v[232:233], v[12:13]
	s_nop 0
	v_cvt_pk_bf16_f32 v11, v12, v13
	v_add_u32_e32 v14, 0x1900, v1
	v_mov_b32_e32 v15, v3
	v_add_u32_e32 v2, 0x1900, v0
	v_lshlrev_b64 v[12:13], 11, v[14:15]
	v_lshlrev_b64 v[14:15], 11, v[2:3]
	v_lshl_add_u64 v[14:15], s[4:5], 0, v[14:15]
	v_lshl_add_u64 v[12:13], s[4:5], 0, v[12:13]
	global_store_short v[14:15], v11, off offset:1024
	global_store_short_d16_hi v[12:13], v11, off offset:1024
	v_lshrrev_b32_e32 v13, 6, v8
	v_lshrrev_b32_e32 v11, 1, v8
	v_lshrrev_b32_e32 v12, 6, v9
	v_and_b32_e32 v13, 0x80, v13
	v_lshrrev_b32_e32 v15, 8, v8
	v_and_b32_e32 v17, 0x60, v8
	v_lshrrev_b32_e32 v2, 1, v9
	v_and_b32_e32 v11, 12, v11
	v_and_b32_e32 v12, 0x80, v12
	v_lshrrev_b32_e32 v14, 8, v9
	v_and_b32_e32 v15, 16, v15
	v_and_b32_e32 v16, 0x60, v9
	v_or_b32_e32 v13, v13, v17
	v_and_b32_e32 v2, 12, v2
	v_or_b32_e32 v11, v146, v11
	v_and_b32_e32 v14, 16, v14
	v_or_b32_e32 v12, v12, v16
	v_or_b32_e32 v13, v13, v15
	v_or_b32_e32 v2, v145, v2
	v_or_b32_e32 v12, v12, v14
	v_or_b32_e32 v11, v13, v11
	v_lshlrev_b32_e32 v13, 3, v8
	v_or_b32_e32 v2, v12, v2
	v_lshlrev_b32_e32 v12, 3, v9
	v_and_b32_e32 v13, 32, v13
	v_lshrrev_b32_e32 v14, 5, v8
	v_and_b32_e32 v12, 32, v12
	v_lshl_add_u32 v11, v11, 8, 0
	v_and_b32_e32 v14, 0x7c, v14
	v_lshrrev_b32_e32 v15, 5, v9
	v_lshlrev_b32_e32 v13, 2, v13
	v_lshl_add_u32 v2, v2, 8, 0
	v_and_b32_e32 v15, 0x7c, v15
	v_add3_u32 v11, v11, v14, v13
	v_lshlrev_b32_e32 v12, 2, v12
	v_add3_u32 v2, v2, v15, v12
	ds_read_b32 v12, v11 offset:16
	ds_read_b32 v13, v2 offset:16
	v_add_u32_e32 v11, 0x10010, v11
	v_add_u32_e32 v2, 0x10010, v2
	ds_read_b32 v14, v11
	ds_read_b32 v15, v2
	v_add_u32_e32 v2, 0x100, v8
	v_lshl_add_u64 v[18:19], s[0:1], 0, v[2:3]
	v_lshlrev_b64 v[18:19], 2, v[18:19]
	v_lshl_add_u64 v[20:21], s[60:61], 0, v[18:19]
	s_waitcnt lgkmcnt(0)
	v_pk_add_f32 v[236:237], v[12:13], v[14:15]
	v_add_u32_e32 v14, 0x100, v9
	v_mov_b32_e32 v15, v3
	v_lshl_add_u64 v[16:17], s[2:3], 0, v[14:15]
	v_lshlrev_b64 v[16:17], 2, v[16:17]
	v_lshl_add_u64 v[18:19], s[58:59], 0, v[18:19]
	v_lshl_add_u64 v[22:23], s[60:61], 0, v[16:17]
	global_load_dword v232, v[20:21], off
	s_nop 0
	global_load_dword v233, v[22:23], off
	v_lshl_add_u64 v[16:17], s[58:59], 0, v[16:17]
	global_load_dword v234, v[18:19], off
	s_nop 0
	global_load_dword v235, v[16:17], off
	v_add_u32_e32 v9, 0x400, v9
	v_add_u32_e32 v8, 0x400, v8
	s_waitcnt vmcnt(18)
; __device__ __forceinline__ bfr f2bf(float f) { return (bfr)(pack2(f, 0.f) & 0xffffu); }
; __device__ __forceinline__ void phase_longconv(const Params& P, unsigned char* smraw, int bid, int nb) {
;     ...
;                 for (int t = tid; t < LSEQ; t += NTHR) {
;                     const int b = t & 127, a_ = t >> 7;
;                     const int bt = b >> 5, rb = b & 31, at = a_ >> 5;
;                     const int hh = (rb >> 2) & 1, q = (rb & 3) + 4 * (rb >> 3);
;                     const int w = (bt >> 1) + 2 * (at >> 1);
;                     const int idx = (w * 64 + ((bt & 1) * 2 + (at & 1)) * 16 + q) * 64 + (a_ & 31) + 32 * hh;
;                     const float v = Red[idx] + Red[idx + 4 * 64 * 64];
;                     const int row = NCTX + t;
;                     const float x0 = X0[(size_t)c * NT + row];
;                     const float y = x0 * (v * nrm + Z[(size_t)c * NT + row] * sk);
;                     ATT[(size_t)row * 1024 + 512 + c] = f2bf(y);
;                 }
	v_pk_mul_f32 v[16:17], v[6:7], v[240:241]
	s_nop 0
	v_pk_fma_f32 v[12:13], v[4:5], v[242:243], v[16:17]
	s_nop 0
	v_pk_mul_f32 v[12:13], v[238:239], v[12:13]
	s_nop 0
	v_cvt_pk_bf16_f32 v11, v12, v13
	v_add_u32_e32 v14, 0x1d00, v1
	v_mov_b32_e32 v15, v3
	v_add_u32_e32 v2, 0x1d00, v0
	v_lshlrev_b64 v[12:13], 11, v[14:15]
	v_lshlrev_b64 v[14:15], 11, v[2:3]
	v_lshl_add_u64 v[14:15], s[4:5], 0, v[14:15]
	v_lshl_add_u64 v[12:13], s[4:5], 0, v[12:13]
	global_store_short v[14:15], v11, off offset:1024
	global_store_short_d16_hi v[12:13], v11, off offset:1024
	v_lshrrev_b32_e32 v13, 6, v8
	v_lshrrev_b32_e32 v11, 1, v8
	v_lshrrev_b32_e32 v12, 6, v9
	v_and_b32_e32 v13, 0x80, v13
	v_lshrrev_b32_e32 v15, 8, v8
	v_and_b32_e32 v17, 0x60, v8
	v_lshrrev_b32_e32 v2, 1, v9
	v_and_b32_e32 v11, 12, v11
	v_and_b32_e32 v12, 0x80, v12
	v_lshrrev_b32_e32 v14, 8, v9
	v_and_b32_e32 v15, 16, v15
	v_and_b32_e32 v16, 0x60, v9
	v_or_b32_e32 v13, v13, v17
	v_and_b32_e32 v2, 12, v2
	v_or_b32_e32 v11, v146, v11
	v_and_b32_e32 v14, 16, v14
	v_or_b32_e32 v12, v12, v16
	v_or_b32_e32 v13, v13, v15
	v_or_b32_e32 v2, v145, v2
	v_or_b32_e32 v12, v12, v14
	v_or_b32_e32 v11, v13, v11
	v_lshlrev_b32_e32 v13, 3, v8
	v_or_b32_e32 v2, v12, v2
	v_lshlrev_b32_e32 v12, 3, v9
	v_and_b32_e32 v13, 32, v13
	v_lshrrev_b32_e32 v14, 5, v8
	v_and_b32_e32 v12, 32, v12
	v_lshl_add_u32 v11, v11, 8, 0
	v_and_b32_e32 v14, 0x7c, v14
	v_lshrrev_b32_e32 v15, 5, v9
	v_lshlrev_b32_e32 v13, 2, v13
	v_lshl_add_u32 v2, v2, 8, 0
	v_and_b32_e32 v15, 0x7c, v15
	v_add3_u32 v11, v11, v14, v13
	v_lshlrev_b32_e32 v12, 2, v12
	v_add3_u32 v2, v2, v15, v12
	ds_read_b32 v12, v11 offset:16
	ds_read_b32 v13, v2 offset:16
	v_add_u32_e32 v11, 0x10010, v11
	v_add_u32_e32 v2, 0x10010, v2
	ds_read_b32 v14, v11
	ds_read_b32 v15, v2
	v_add_u32_e32 v2, 0x100, v8
	v_lshl_add_u64 v[18:19], s[0:1], 0, v[2:3]
	v_lshlrev_b64 v[18:19], 2, v[18:19]
	v_lshl_add_u64 v[20:21], s[60:61], 0, v[18:19]
	s_waitcnt lgkmcnt(0)
	v_pk_add_f32 v[242:243], v[12:13], v[14:15]
	v_add_u32_e32 v14, 0x100, v9
	v_mov_b32_e32 v15, v3
	v_lshl_add_u64 v[16:17], s[2:3], 0, v[14:15]
	v_lshlrev_b64 v[16:17], 2, v[16:17]
	v_lshl_add_u64 v[18:19], s[58:59], 0, v[18:19]
	v_lshl_add_u64 v[22:23], s[60:61], 0, v[16:17]
	global_load_dword v238, v[20:21], off
	s_nop 0
	global_load_dword v239, v[22:23], off
	v_lshl_add_u64 v[16:17], s[58:59], 0, v[16:17]
	global_load_dword v240, v[18:19], off
	s_nop 0
	global_load_dword v241, v[16:17], off
	v_add_u32_e32 v9, 0x400, v9
	v_add_u32_e32 v8, 0x400, v8
	s_waitcnt vmcnt(18)
	v_pk_mul_f32 v[16:17], v[6:7], v[222:223]
	s_nop 0
	v_pk_fma_f32 v[12:13], v[4:5], v[224:225], v[16:17]
	s_nop 0
	v_pk_mul_f32 v[12:13], v[220:221], v[12:13]
	s_nop 0
	v_cvt_pk_bf16_f32 v11, v12, v13
	v_add_u32_e32 v14, 0x2100, v1
	v_mov_b32_e32 v15, v3
	v_add_u32_e32 v2, 0x2100, v0
	v_lshlrev_b64 v[12:13], 11, v[14:15]
	v_lshlrev_b64 v[14:15], 11, v[2:3]
	v_lshl_add_u64 v[14:15], s[4:5], 0, v[14:15]
	v_lshl_add_u64 v[12:13], s[4:5], 0, v[12:13]
	global_store_short v[14:15], v11, off offset:1024
	global_store_short_d16_hi v[12:13], v11, off offset:1024
	v_lshrrev_b32_e32 v13, 6, v8
	v_lshrrev_b32_e32 v11, 1, v8
	v_lshrrev_b32_e32 v12, 6, v9
	v_and_b32_e32 v13, 0x80, v13
	v_lshrrev_b32_e32 v15, 8, v8
	v_and_b32_e32 v17, 0x60, v8
	v_lshrrev_b32_e32 v2, 1, v9
	v_and_b32_e32 v11, 12, v11
	v_and_b32_e32 v12, 0x80, v12
	v_lshrrev_b32_e32 v14, 8, v9
	v_and_b32_e32 v15, 16, v15
	v_and_b32_e32 v16, 0x60, v9
	v_or_b32_e32 v13, v13, v17
	v_and_b32_e32 v2, 12, v2
	v_or_b32_e32 v11, v146, v11
	v_and_b32_e32 v14, 16, v14
	v_or_b32_e32 v12, v12, v16
	v_or_b32_e32 v13, v13, v15
	v_or_b32_e32 v2, v145, v2
	v_or_b32_e32 v12, v12, v14
	v_or_b32_e32 v11, v13, v11
	v_lshlrev_b32_e32 v13, 3, v8
	v_or_b32_e32 v2, v12, v2
	v_lshlrev_b32_e32 v12, 3, v9
	v_and_b32_e32 v13, 32, v13
	v_lshrrev_b32_e32 v14, 5, v8
	v_and_b32_e32 v12, 32, v12
	v_lshl_add_u32 v11, v11, 8, 0
	v_and_b32_e32 v14, 0x7c, v14
	v_lshrrev_b32_e32 v15, 5, v9
	v_lshlrev_b32_e32 v13, 2, v13
	v_lshl_add_u32 v2, v2, 8, 0
	v_and_b32_e32 v15, 0x7c, v15
	v_add3_u32 v11, v11, v14, v13
	v_lshlrev_b32_e32 v12, 2, v12
	v_add3_u32 v2, v2, v15, v12
	ds_read_b32 v12, v11 offset:16
	ds_read_b32 v13, v2 offset:16
	v_add_u32_e32 v11, 0x10010, v11
	v_add_u32_e32 v2, 0x10010, v2
	ds_read_b32 v14, v11
	ds_read_b32 v15, v2
	v_add_u32_e32 v2, 0x100, v8
	v_lshl_add_u64 v[18:19], s[0:1], 0, v[2:3]
	v_lshlrev_b64 v[18:19], 2, v[18:19]
	v_lshl_add_u64 v[20:21], s[60:61], 0, v[18:19]
	s_waitcnt lgkmcnt(0)
	v_pk_add_f32 v[224:225], v[12:13], v[14:15]
	v_add_u32_e32 v14, 0x100, v9
	v_mov_b32_e32 v15, v3
	v_lshl_add_u64 v[16:17], s[2:3], 0, v[14:15]
	v_lshlrev_b64 v[16:17], 2, v[16:17]
	v_lshl_add_u64 v[18:19], s[58:59], 0, v[18:19]
	v_lshl_add_u64 v[22:23], s[60:61], 0, v[16:17]
	global_load_dword v220, v[20:21], off
	s_nop 0
	global_load_dword v221, v[22:23], off
	v_lshl_add_u64 v[16:17], s[58:59], 0, v[16:17]
	global_load_dword v222, v[18:19], off
	s_nop 0
	global_load_dword v223, v[16:17], off
	v_add_u32_e32 v9, 0x400, v9
	v_add_u32_e32 v8, 0x400, v8
	s_waitcnt vmcnt(18)
; __device__ __forceinline__ bfr f2bf(float f) { return (bfr)(pack2(f, 0.f) & 0xffffu); }
; __device__ __forceinline__ void phase_longconv(const Params& P, unsigned char* smraw, int bid, int nb) {
;     ...
;                 for (int t = tid; t < LSEQ; t += NTHR) {
;                     const int b = t & 127, a_ = t >> 7;
;                     const int bt = b >> 5, rb = b & 31, at = a_ >> 5;
;                     const int hh = (rb >> 2) & 1, q = (rb & 3) + 4 * (rb >> 3);
;                     const int w = (bt >> 1) + 2 * (at >> 1);
;                     const int idx = (w * 64 + ((bt & 1) * 2 + (at & 1)) * 16 + q) * 64 + (a_ & 31) + 32 * hh;
;                     const float v = Red[idx] + Red[idx + 4 * 64 * 64];
;                     const int row = NCTX + t;
;                     const float x0 = X0[(size_t)c * NT + row];
;                     const float y = x0 * (v * nrm + Z[(size_t)c * NT + row] * sk);
;                     ATT[(size_t)row * 1024 + 512 + c] = f2bf(y);
;                 }
	v_pk_mul_f32 v[16:17], v[6:7], v[228:229]
	s_nop 0
	v_pk_fma_f32 v[12:13], v[4:5], v[230:231], v[16:17]
	s_nop 0
	v_pk_mul_f32 v[12:13], v[226:227], v[12:13]
	s_nop 0
	v_cvt_pk_bf16_f32 v11, v12, v13
	v_add_u32_e32 v14, 0x2500, v1
	v_mov_b32_e32 v15, v3
	v_add_u32_e32 v2, 0x2500, v0
	v_lshlrev_b64 v[12:13], 11, v[14:15]
	v_lshlrev_b64 v[14:15], 11, v[2:3]
	v_lshl_add_u64 v[14:15], s[4:5], 0, v[14:15]
	v_lshl_add_u64 v[12:13], s[4:5], 0, v[12:13]
	global_store_short v[14:15], v11, off offset:1024
	global_store_short_d16_hi v[12:13], v11, off offset:1024
	v_lshrrev_b32_e32 v13, 6, v8
	v_lshrrev_b32_e32 v11, 1, v8
	v_lshrrev_b32_e32 v12, 6, v9
	v_and_b32_e32 v13, 0x80, v13
	v_lshrrev_b32_e32 v15, 8, v8
	v_and_b32_e32 v17, 0x60, v8
	v_lshrrev_b32_e32 v2, 1, v9
	v_and_b32_e32 v11, 12, v11
	v_and_b32_e32 v12, 0x80, v12
	v_lshrrev_b32_e32 v14, 8, v9
	v_and_b32_e32 v15, 16, v15
	v_and_b32_e32 v16, 0x60, v9
	v_or_b32_e32 v13, v13, v17
	v_and_b32_e32 v2, 12, v2
	v_or_b32_e32 v11, v146, v11
	v_and_b32_e32 v14, 16, v14
	v_or_b32_e32 v12, v12, v16
	v_or_b32_e32 v13, v13, v15
	v_or_b32_e32 v2, v145, v2
	v_or_b32_e32 v12, v12, v14
	v_or_b32_e32 v11, v13, v11
	v_lshlrev_b32_e32 v13, 3, v8
	v_or_b32_e32 v2, v12, v2
	v_lshlrev_b32_e32 v12, 3, v9
	v_and_b32_e32 v13, 32, v13
	v_lshrrev_b32_e32 v14, 5, v8
	v_and_b32_e32 v12, 32, v12
	v_lshl_add_u32 v11, v11, 8, 0
	v_and_b32_e32 v14, 0x7c, v14
	v_lshrrev_b32_e32 v15, 5, v9
	v_lshlrev_b32_e32 v13, 2, v13
	v_lshl_add_u32 v2, v2, 8, 0
	v_and_b32_e32 v15, 0x7c, v15
	v_add3_u32 v11, v11, v14, v13
	v_lshlrev_b32_e32 v12, 2, v12
	v_add3_u32 v2, v2, v15, v12
	ds_read_b32 v12, v11 offset:16
	ds_read_b32 v13, v2 offset:16
	v_add_u32_e32 v11, 0x10010, v11
	v_add_u32_e32 v2, 0x10010, v2
	ds_read_b32 v14, v11
	ds_read_b32 v15, v2
	v_add_u32_e32 v2, 0x100, v8
	v_lshl_add_u64 v[18:19], s[0:1], 0, v[2:3]
	v_lshlrev_b64 v[18:19], 2, v[18:19]
	v_lshl_add_u64 v[20:21], s[60:61], 0, v[18:19]
	s_waitcnt lgkmcnt(0)
	v_pk_add_f32 v[230:231], v[12:13], v[14:15]
	v_add_u32_e32 v14, 0x100, v9
	v_mov_b32_e32 v15, v3
	v_lshl_add_u64 v[16:17], s[2:3], 0, v[14:15]
	v_lshlrev_b64 v[16:17], 2, v[16:17]
	v_lshl_add_u64 v[18:19], s[58:59], 0, v[18:19]
	v_lshl_add_u64 v[22:23], s[60:61], 0, v[16:17]
	global_load_dword v226, v[20:21], off
	s_nop 0
	global_load_dword v227, v[22:23], off
	v_lshl_add_u64 v[16:17], s[58:59], 0, v[16:17]
	global_load_dword v228, v[18:19], off
	s_nop 0
	global_load_dword v229, v[16:17], off
	v_add_u32_e32 v9, 0x400, v9
	v_add_u32_e32 v8, 0x400, v8
	s_waitcnt vmcnt(18)
	v_pk_mul_f32 v[16:17], v[6:7], v[234:235]
	s_nop 0
	v_pk_fma_f32 v[12:13], v[4:5], v[236:237], v[16:17]
	s_nop 0
	v_pk_mul_f32 v[12:13], v[232:233], v[12:13]
	s_nop 0
	v_cvt_pk_bf16_f32 v11, v12, v13
	v_add_u32_e32 v14, 0x2900, v1
	v_mov_b32_e32 v15, v3
	v_add_u32_e32 v2, 0x2900, v0
	v_lshlrev_b64 v[12:13], 11, v[14:15]
	v_lshlrev_b64 v[14:15], 11, v[2:3]
	v_lshl_add_u64 v[14:15], s[4:5], 0, v[14:15]
	v_lshl_add_u64 v[12:13], s[4:5], 0, v[12:13]
	global_store_short v[14:15], v11, off offset:1024
	global_store_short_d16_hi v[12:13], v11, off offset:1024
	v_lshrrev_b32_e32 v13, 6, v8
	v_lshrrev_b32_e32 v11, 1, v8
	v_lshrrev_b32_e32 v12, 6, v9
	v_and_b32_e32 v13, 0x80, v13
	v_lshrrev_b32_e32 v15, 8, v8
	v_and_b32_e32 v17, 0x60, v8
	v_lshrrev_b32_e32 v2, 1, v9
	v_and_b32_e32 v11, 12, v11
	v_and_b32_e32 v12, 0x80, v12
	v_lshrrev_b32_e32 v14, 8, v9
	v_and_b32_e32 v15, 16, v15
	v_and_b32_e32 v16, 0x60, v9
	v_or_b32_e32 v13, v13, v17
	v_and_b32_e32 v2, 12, v2
	v_or_b32_e32 v11, v146, v11
	v_and_b32_e32 v14, 16, v14
	v_or_b32_e32 v12, v12, v16
	v_or_b32_e32 v13, v13, v15
	v_or_b32_e32 v2, v145, v2
	v_or_b32_e32 v12, v12, v14
	v_or_b32_e32 v11, v13, v11
	v_lshlrev_b32_e32 v13, 3, v8
	v_or_b32_e32 v2, v12, v2
	v_lshlrev_b32_e32 v12, 3, v9
	v_and_b32_e32 v13, 32, v13
	v_lshrrev_b32_e32 v14, 5, v8
	v_and_b32_e32 v12, 32, v12
	v_lshl_add_u32 v11, v11, 8, 0
	v_and_b32_e32 v14, 0x7c, v14
	v_lshrrev_b32_e32 v15, 5, v9
	v_lshlrev_b32_e32 v13, 2, v13
	v_lshl_add_u32 v2, v2, 8, 0
	v_and_b32_e32 v15, 0x7c, v15
	v_add3_u32 v11, v11, v14, v13
	v_lshlrev_b32_e32 v12, 2, v12
	v_add3_u32 v2, v2, v15, v12
	ds_read_b32 v12, v11 offset:16
	ds_read_b32 v13, v2 offset:16
	v_add_u32_e32 v11, 0x10010, v11
	v_add_u32_e32 v2, 0x10010, v2
	ds_read_b32 v14, v11
	ds_read_b32 v15, v2
	v_add_u32_e32 v2, 0x100, v8
	v_lshl_add_u64 v[18:19], s[0:1], 0, v[2:3]
	v_lshlrev_b64 v[18:19], 2, v[18:19]
	v_lshl_add_u64 v[20:21], s[60:61], 0, v[18:19]
	s_waitcnt lgkmcnt(0)
	v_pk_add_f32 v[236:237], v[12:13], v[14:15]
	v_add_u32_e32 v14, 0x100, v9
	v_mov_b32_e32 v15, v3
	v_lshl_add_u64 v[16:17], s[2:3], 0, v[14:15]
	v_lshlrev_b64 v[16:17], 2, v[16:17]
	v_lshl_add_u64 v[18:19], s[58:59], 0, v[18:19]
	v_lshl_add_u64 v[22:23], s[60:61], 0, v[16:17]
	global_load_dword v232, v[20:21], off
	s_nop 0
	global_load_dword v233, v[22:23], off
	v_lshl_add_u64 v[16:17], s[58:59], 0, v[16:17]
	global_load_dword v234, v[18:19], off
	s_nop 0
	global_load_dword v235, v[16:17], off
	v_add_u32_e32 v9, 0x400, v9
	v_add_u32_e32 v8, 0x400, v8
	s_waitcnt vmcnt(18)
; __device__ __forceinline__ bfr f2bf(float f) { return (bfr)(pack2(f, 0.f) & 0xffffu); }
; __device__ __forceinline__ void phase_longconv(const Params& P, unsigned char* smraw, int bid, int nb) {
;     ...
;                 for (int t = tid; t < LSEQ; t += NTHR) {
;                     const int b = t & 127, a_ = t >> 7;
;                     const int bt = b >> 5, rb = b & 31, at = a_ >> 5;
;                     const int hh = (rb >> 2) & 1, q = (rb & 3) + 4 * (rb >> 3);
;                     const int w = (bt >> 1) + 2 * (at >> 1);
;                     const int idx = (w * 64 + ((bt & 1) * 2 + (at & 1)) * 16 + q) * 64 + (a_ & 31) + 32 * hh;
;                     const float v = Red[idx] + Red[idx + 4 * 64 * 64];
;                     const int row = NCTX + t;
;                     const float x0 = X0[(size_t)c * NT + row];
;                     const float y = x0 * (v * nrm + Z[(size_t)c * NT + row] * sk);
;                     ATT[(size_t)row * 1024 + 512 + c] = f2bf(y);
;                 }
;             }
;         }
;     ...
;     }
;     {
;         float* zs = (float*)smraw; float* hw = zs + 512;
;         for (int c = bid; c < 512; c += nb) {
;             __syncthreads();
;             if (tid < 256) zs[tid] = Z[(size_t)c * NT + tid];
	v_pk_mul_f32 v[16:17], v[6:7], v[240:241]
	s_nop 0
	v_pk_fma_f32 v[12:13], v[4:5], v[242:243], v[16:17]
	s_nop 0
	v_pk_mul_f32 v[12:13], v[238:239], v[12:13]
	s_nop 0
	v_cvt_pk_bf16_f32 v11, v12, v13
	v_add_u32_e32 v14, 0x2d00, v1
	v_mov_b32_e32 v15, v3
	v_add_u32_e32 v2, 0x2d00, v0
	v_lshlrev_b64 v[12:13], 11, v[14:15]
	v_lshlrev_b64 v[14:15], 11, v[2:3]
	v_lshl_add_u64 v[14:15], s[4:5], 0, v[14:15]
	v_lshl_add_u64 v[12:13], s[4:5], 0, v[12:13]
	global_store_short v[14:15], v11, off offset:1024
	global_store_short_d16_hi v[12:13], v11, off offset:1024
	v_lshrrev_b32_e32 v13, 6, v8
	v_lshrrev_b32_e32 v11, 1, v8
	v_lshrrev_b32_e32 v12, 6, v9
	v_and_b32_e32 v13, 0x80, v13
	v_lshrrev_b32_e32 v15, 8, v8
	v_and_b32_e32 v17, 0x60, v8
	v_lshrrev_b32_e32 v2, 1, v9
	v_and_b32_e32 v11, 12, v11
	v_and_b32_e32 v12, 0x80, v12
	v_lshrrev_b32_e32 v14, 8, v9
	v_and_b32_e32 v15, 16, v15
	v_and_b32_e32 v16, 0x60, v9
	v_or_b32_e32 v13, v13, v17
	v_and_b32_e32 v2, 12, v2
	v_or_b32_e32 v11, v146, v11
	v_and_b32_e32 v14, 16, v14
	v_or_b32_e32 v12, v12, v16
	v_or_b32_e32 v13, v13, v15
	v_or_b32_e32 v2, v145, v2
	v_or_b32_e32 v12, v12, v14
	v_or_b32_e32 v11, v13, v11
	v_lshlrev_b32_e32 v13, 3, v8
	v_or_b32_e32 v2, v12, v2
	v_lshlrev_b32_e32 v12, 3, v9
	v_and_b32_e32 v13, 32, v13
	v_lshrrev_b32_e32 v14, 5, v8
	v_and_b32_e32 v12, 32, v12
	v_lshl_add_u32 v11, v11, 8, 0
	v_and_b32_e32 v14, 0x7c, v14
	v_lshrrev_b32_e32 v15, 5, v9
	v_lshlrev_b32_e32 v13, 2, v13
	v_lshl_add_u32 v2, v2, 8, 0
	v_and_b32_e32 v15, 0x7c, v15
	v_add3_u32 v11, v11, v14, v13
	v_lshlrev_b32_e32 v12, 2, v12
	v_add3_u32 v2, v2, v15, v12
	ds_read_b32 v12, v11 offset:16
	ds_read_b32 v13, v2 offset:16
	v_add_u32_e32 v11, 0x10010, v11
	v_add_u32_e32 v2, 0x10010, v2
	ds_read_b32 v14, v11
	ds_read_b32 v15, v2
	v_add_u32_e32 v2, 0x100, v8
	v_lshl_add_u64 v[18:19], s[0:1], 0, v[2:3]
	v_lshlrev_b64 v[18:19], 2, v[18:19]
	v_lshl_add_u64 v[20:21], s[60:61], 0, v[18:19]
	s_waitcnt lgkmcnt(0)
	v_pk_add_f32 v[242:243], v[12:13], v[14:15]
	v_add_u32_e32 v14, 0x100, v9
	v_mov_b32_e32 v15, v3
	v_lshl_add_u64 v[16:17], s[2:3], 0, v[14:15]
	v_lshlrev_b64 v[16:17], 2, v[16:17]
	v_lshl_add_u64 v[18:19], s[58:59], 0, v[18:19]
	v_lshl_add_u64 v[22:23], s[60:61], 0, v[16:17]
	global_load_dword v238, v[20:21], off
	s_nop 0
	global_load_dword v239, v[22:23], off
	v_lshl_add_u64 v[16:17], s[58:59], 0, v[16:17]
	global_load_dword v240, v[18:19], off
	s_nop 0
	global_load_dword v241, v[16:17], off
	v_add_u32_e32 v9, 0x400, v9
	v_add_u32_e32 v8, 0x400, v8
	s_waitcnt vmcnt(18)
	v_pk_mul_f32 v[16:17], v[6:7], v[222:223]
	s_nop 0
	v_pk_fma_f32 v[12:13], v[4:5], v[224:225], v[16:17]
	s_nop 0
	v_pk_mul_f32 v[12:13], v[220:221], v[12:13]
	s_nop 0
	v_cvt_pk_bf16_f32 v11, v12, v13
	v_add_u32_e32 v14, 0x3100, v1
	v_mov_b32_e32 v15, v3
	v_add_u32_e32 v2, 0x3100, v0
	v_lshlrev_b64 v[12:13], 11, v[14:15]
	v_lshlrev_b64 v[14:15], 11, v[2:3]
	v_lshl_add_u64 v[14:15], s[4:5], 0, v[14:15]
	v_lshl_add_u64 v[12:13], s[4:5], 0, v[12:13]
	global_store_short v[14:15], v11, off offset:1024
	global_store_short_d16_hi v[12:13], v11, off offset:1024
	s_waitcnt vmcnt(14)
	v_pk_mul_f32 v[16:17], v[6:7], v[228:229]
	s_nop 0
	v_pk_fma_f32 v[12:13], v[4:5], v[230:231], v[16:17]
	s_nop 0
	v_pk_mul_f32 v[12:13], v[226:227], v[12:13]
	s_nop 0
	v_cvt_pk_bf16_f32 v11, v12, v13
	v_add_u32_e32 v14, 0x3500, v1
	v_mov_b32_e32 v15, v3
	v_add_u32_e32 v2, 0x3500, v0
	v_lshlrev_b64 v[12:13], 11, v[14:15]
	v_lshlrev_b64 v[14:15], 11, v[2:3]
	v_lshl_add_u64 v[14:15], s[4:5], 0, v[14:15]
	v_lshl_add_u64 v[12:13], s[4:5], 0, v[12:13]
	global_store_short v[14:15], v11, off offset:1024
	global_store_short_d16_hi v[12:13], v11, off offset:1024
	s_waitcnt vmcnt(10)
	v_pk_mul_f32 v[16:17], v[6:7], v[234:235]
	s_nop 0
	v_pk_fma_f32 v[12:13], v[4:5], v[236:237], v[16:17]
	s_nop 0
	v_pk_mul_f32 v[12:13], v[232:233], v[12:13]
	s_nop 0
	v_cvt_pk_bf16_f32 v11, v12, v13
	v_add_u32_e32 v14, 0x3900, v1
	v_mov_b32_e32 v15, v3
	v_add_u32_e32 v2, 0x3900, v0
	v_lshlrev_b64 v[12:13], 11, v[14:15]
	v_lshlrev_b64 v[14:15], 11, v[2:3]
	v_lshl_add_u64 v[14:15], s[4:5], 0, v[14:15]
	v_lshl_add_u64 v[12:13], s[4:5], 0, v[12:13]
	global_store_short v[14:15], v11, off offset:1024
	global_store_short_d16_hi v[12:13], v11, off offset:1024
	s_waitcnt vmcnt(6)
	v_pk_mul_f32 v[16:17], v[6:7], v[240:241]
	s_nop 0
	v_pk_fma_f32 v[12:13], v[4:5], v[242:243], v[16:17]
	s_nop 0
	v_pk_mul_f32 v[12:13], v[238:239], v[12:13]
	s_nop 0
	v_cvt_pk_bf16_f32 v11, v12, v13
	v_add_u32_e32 v14, 0x3d00, v1
	v_mov_b32_e32 v15, v3
	v_add_u32_e32 v2, 0x3d00, v0
	v_lshlrev_b64 v[12:13], 11, v[14:15]
	v_lshlrev_b64 v[14:15], 11, v[2:3]
	v_lshl_add_u64 v[14:15], s[4:5], 0, v[14:15]
	v_lshl_add_u64 v[12:13], s[4:5], 0, v[12:13]
	global_store_short v[14:15], v11, off offset:1024
	global_store_short_d16_hi v[12:13], v11, off offset:1024
	s_or_b64 exec, exec, s[48:49]
	s_mov_b64 s[0:1], exec
	s_mov_b64 s[2:3], 0
	v_readlane_b32 s76, v252, 19
	s_and_b64 s[2:3], s[0:1], s[2:3]
	v_readlane_b32 s78, v252, 21
	v_readlane_b32 s79, v252, 22
	v_readlane_b32 s77, v252, 20
	s_mov_b64 exec, s[2:3]
	s_cbranch_execz .LBB0_762
	v_mov_b32_e32 v5, v6
	s_mov_b64 s[2:3], 0
	v_mov_b32_e32 v2, v211
	v_mov_b32_e32 v10, v210
	v_mov_b32_e32 v11, v209
	v_mov_b32_e32 v12, v208
	v_mov_b32_e32 v13, v207
	v_mov_b64_e32 v[6:7], v[168:169]
	v_mov_b64_e32 v[8:9], v[166:167]
	v_mov_b32_e32 v14, v204

; __device__ __forceinline__ float bf2f(bfr h) { return __uint_as_float(((unsigned)h) << 16); }
; __device__ __forceinline__ unsigned char f2fp8(float f) { return (unsigned char)(__builtin_amdgcn_cvt_pk_fp8_f32(f, f, 0, false) & 0xff); }
; __device__ __forceinline__ void phase_qkprep_s5a(const Params& P, float* sm, int bid, int nb) {
;     ...
;     for (int row = gw; row < NT; row += nw) {
;         const bool lat = row >= NCTX;
;         float cs = 1.f, sn = 0.f;
;         if (lat) {
;             const int t = row - NCTX;
;             const float ang = (float)((lane < 32) ? (t >> 6) : (t & 63)) * invf;
;             cs = __cosf(ang); sn = __sinf(ang);
;         }
;         const bfr* src = QK + (size_t)row * 1280 + lane;
; #pragma unroll
;         for (int slot = lat ? 0 : 8; slot < 10; ++slot) {
;             const float x = bf2f(src[slot * 64]);
;             const float ss = wave_sum(x * x);
;             float y = x * rsqrtf(ss * (1.f / 64.f) + 1e-6f) * (slot < 8 ? qg : kg);
;             if (lat) {
;                 const float other = __shfl_xor(y, 1, 64);
;                 y = (lane & 1) ? (other * sn + y * cs) : (y * cs - other * sn);
;             }
;             if (slot < 8) QN[(size_t)(row - NCTX) * 512 + slot * 64 + lane] = f2fp8(y * (0.5f * 1.4426950408889634f));
;             else KN[(size_t)row * 128 + (slot - 8) * 64 + lane] = f2fp8(y * 0.25f);
;         }
.LBB0_1808:
	s_or_b64 exec, exec, s[0:1]
	v_ashrrev_i32_e32 v11, 31, v10
	v_lshlrev_b32_e32 v4, 7, v29
	v_lshlrev_b64 v[16:17], 9, v[10:11]
	v_lshl_add_u64 v[14:15], v[6:7], 0, v[4:5]
	v_lshlrev_b32_e32 v4, 6, v29
	v_lshl_add_u64 v[16:17], v[16:17], 0, v[4:5]
	v_lshl_add_u64 v[16:17], v[8:9], 0, v[16:17]
	v_lshl_add_u64 v[18:19], v[12:13], 0, v[4:5]
	v_readfirstlane_b32 s98, v29
	s_cmp_eq_u32 s98, 0
	s_cbranch_scc0 .Lqk_ctxrow
	global_load_ushort v110, v[14:15], off
	global_load_ushort v111, v[14:15], off offset:128
	global_load_ushort v112, v[14:15], off offset:256
	global_load_ushort v113, v[14:15], off offset:384
	global_load_ushort v114, v[14:15], off offset:512
	global_load_ushort v115, v[14:15], off offset:640
	global_load_ushort v116, v[14:15], off offset:768
	global_load_ushort v117, v[14:15], off offset:896
	global_load_ushort v118, v[14:15], off offset:1024
	global_load_ushort v119, v[14:15], off offset:1152
	v_mov_b32_e32 v11, 0
	v_mov_b32_e32 v30, 0
	s_waitcnt vmcnt(9)
	v_lshlrev_b32_e32 v4, 16, v110
	v_mul_f32_e32 v31, v4, v4
	s_nop 1
	v_mov_b32_dpp v31, v31 row_shr:1 row_mask:0xf bank_mask:0xf bound_ctrl:1
	v_fmac_f32_e32 v31, v4, v4
	s_nop 1
	v_add_f32_dpp v31, v31, v31 row_shr:2 row_mask:0xf bank_mask:0xf bound_ctrl:1
	s_nop 1
	v_add_f32_dpp v31, v31, v31 row_shr:4 row_mask:0xf bank_mask:0xf bound_ctrl:1
	s_nop 1
	v_add_f32_dpp v31, v31, v31 row_shr:8 row_mask:0xf bank_mask:0xf bound_ctrl:1
	s_nop 1
	v_mov_b32_dpp v11, v31 row_bcast:15 row_mask:0xa bank_mask:0xf bound_ctrl:1
	v_add_f32_e32 v11, v31, v11
	s_nop 1
	v_mov_b32_dpp v30, v11 row_bcast:31 row_mask:0xc bank_mask:0xf bound_ctrl:1
	v_add_f32_e32 v11, v11, v30
	s_nop 0
	v_readlane_b32 s0, v11, 63
	s_nop 1
	v_fma_f32 v11, s0, v24, v3
	v_mul_f32_e32 v30, 0x4b800000, v11
	v_cmp_gt_f32_e64 s[8:9], s24, v11
	s_nop 0
	s_nop 0
	v_cndmask_b32_e64 v11, v11, v30, s[8:9]
	v_rsq_f32_e32 v11, v11
	s_nop 0
	v_mul_f32_e32 v30, 0x45800000, v11
	v_cndmask_b32_e64 v11, v11, v30, s[8:9]
	s_nop 0
	v_mul_f32_e32 v4, v11, v4
	s_nop 0
	v_mov_b32_e32 v11, v22
	v_mul_f32_e32 v4, v11, v4
	v_and_b32_e32 v11, 64, v25
	v_add_u32_e32 v11, 64, v11
	v_cmp_lt_i32_e64 s[8:9], v26, v11
	s_nop 1
	v_cndmask_b32_e64 v11, v25, v26, s[8:9]
	v_lshlrev_b32_e32 v11, 2, v11
	ds_bpermute_b32 v11, v11, v4
	s_waitcnt lgkmcnt(0)
	v_mul_f32_e32 v11, v28, v11
	v_cndmask_b32_e64 v11, v11, -v11, s[4:5]
	v_fmac_f32_e32 v11, v27, v4
	v_mov_b32_e32 v4, v11
	v_mul_f32_e32 v4, 0x3f38aa3b, v4
	v_mov_b32_e32 v11, 0
	v_cvt_pk_fp8_f32 v11, v4, v4
	global_store_byte v[16:17], v11, off offset:0
	v_mov_b32_e32 v11, 0
	v_mov_b32_e32 v30, 0
	s_waitcnt vmcnt(9)
	v_lshlrev_b32_e32 v4, 16, v111
	v_mul_f32_e32 v31, v4, v4
	s_nop 1
	v_mov_b32_dpp v31, v31 row_shr:1 row_mask:0xf bank_mask:0xf bound_ctrl:1
	v_fmac_f32_e32 v31, v4, v4
	s_nop 1
	v_add_f32_dpp v31, v31, v31 row_shr:2 row_mask:0xf bank_mask:0xf bound_ctrl:1
	s_nop 1
	v_add_f32_dpp v31, v31, v31 row_shr:4 row_mask:0xf bank_mask:0xf bound_ctrl:1
	s_nop 1
	v_add_f32_dpp v31, v31, v31 row_shr:8 row_mask:0xf bank_mask:0xf bound_ctrl:1
	s_nop 1
	v_mov_b32_dpp v11, v31 row_bcast:15 row_mask:0xa bank_mask:0xf bound_ctrl:1
	v_add_f32_e32 v11, v31, v11
	s_nop 1
	v_mov_b32_dpp v30, v11 row_bcast:31 row_mask:0xc bank_mask:0xf bound_ctrl:1
	v_add_f32_e32 v11, v11, v30
	s_nop 0
	v_readlane_b32 s0, v11, 63
	s_nop 1
	v_fma_f32 v11, s0, v24, v3
	v_mul_f32_e32 v30, 0x4b800000, v11
	v_cmp_gt_f32_e64 s[8:9], s24, v11
	s_nop 0
	s_nop 0
	v_cndmask_b32_e64 v11, v11, v30, s[8:9]
	v_rsq_f32_e32 v11, v11
	s_nop 0
	v_mul_f32_e32 v30, 0x45800000, v11
	v_cndmask_b32_e64 v11, v11, v30, s[8:9]
	s_nop 0
	v_mul_f32_e32 v4, v11, v4
	s_nop 0
	v_mov_b32_e32 v11, v22
	v_mul_f32_e32 v4, v11, v4
	v_and_b32_e32 v11, 64, v25
	v_add_u32_e32 v11, 64, v11
	v_cmp_lt_i32_e64 s[8:9], v26, v11
	s_nop 1
	v_cndmask_b32_e64 v11, v25, v26, s[8:9]
	v_lshlrev_b32_e32 v11, 2, v11
	ds_bpermute_b32 v11, v11, v4
	s_waitcnt lgkmcnt(0)
	v_mul_f32_e32 v11, v28, v11
	v_cndmask_b32_e64 v11, v11, -v11, s[4:5]
	v_fmac_f32_e32 v11, v27, v4
	v_mov_b32_e32 v4, v11
	v_mul_f32_e32 v4, 0x3f38aa3b, v4
	v_mov_b32_e32 v11, 0
	v_cvt_pk_fp8_f32 v11, v4, v4
	global_store_byte v[16:17], v11, off offset:64
	v_mov_b32_e32 v11, 0
	v_mov_b32_e32 v30, 0
	s_waitcnt vmcnt(9)
	v_lshlrev_b32_e32 v4, 16, v112
	v_mul_f32_e32 v31, v4, v4
	s_nop 1
	v_mov_b32_dpp v31, v31 row_shr:1 row_mask:0xf bank_mask:0xf bound_ctrl:1
	v_fmac_f32_e32 v31, v4, v4
	s_nop 1
	v_add_f32_dpp v31, v31, v31 row_shr:2 row_mask:0xf bank_mask:0xf bound_ctrl:1
	s_nop 1
	v_add_f32_dpp v31, v31, v31 row_shr:4 row_mask:0xf bank_mask:0xf bound_ctrl:1
	s_nop 1
	v_add_f32_dpp v31, v31, v31 row_shr:8 row_mask:0xf bank_mask:0xf bound_ctrl:1
	s_nop 1
	v_mov_b32_dpp v11, v31 row_bcast:15 row_mask:0xa bank_mask:0xf bound_ctrl:1
	v_add_f32_e32 v11, v31, v11
	s_nop 1
	v_mov_b32_dpp v30, v11 row_bcast:31 row_mask:0xc bank_mask:0xf bound_ctrl:1
	v_add_f32_e32 v11, v11, v30
	s_nop 0
	v_readlane_b32 s0, v11, 63
	s_nop 1
	v_fma_f32 v11, s0, v24, v3
	v_mul_f32_e32 v30, 0x4b800000, v11
	v_cmp_gt_f32_e64 s[8:9], s24, v11
	s_nop 0
	s_nop 0
	v_cndmask_b32_e64 v11, v11, v30, s[8:9]
	v_rsq_f32_e32 v11, v11
	s_nop 0
	v_mul_f32_e32 v30, 0x45800000, v11
	v_cndmask_b32_e64 v11, v11, v30, s[8:9]
	s_nop 0
	v_mul_f32_e32 v4, v11, v4
	s_nop 0
	v_mov_b32_e32 v11, v22
	v_mul_f32_e32 v4, v11, v4
	v_and_b32_e32 v11, 64, v25
	v_add_u32_e32 v11, 64, v11
	v_cmp_lt_i32_e64 s[8:9], v26, v11
	s_nop 1
	v_cndmask_b32_e64 v11, v25, v26, s[8:9]
	v_lshlrev_b32_e32 v11, 2, v11
	ds_bpermute_b32 v11, v11, v4
	s_waitcnt lgkmcnt(0)
; __device__ __forceinline__ float bf2f(bfr h) { return __uint_as_float(((unsigned)h) << 16); }
; __device__ __forceinline__ unsigned char f2fp8(float f) { return (unsigned char)(__builtin_amdgcn_cvt_pk_fp8_f32(f, f, 0, false) & 0xff); }
; __device__ __forceinline__ void phase_qkprep_s5a(const Params& P, float* sm, int bid, int nb) {
;     ...
;         for (int slot = lat ? 0 : 8; slot < 10; ++slot) {
;             const float x = bf2f(src[slot * 64]);
;             const float ss = wave_sum(x * x);
;             float y = x * rsqrtf(ss * (1.f / 64.f) + 1e-6f) * (slot < 8 ? qg : kg);
;             if (lat) {
;                 const float other = __shfl_xor(y, 1, 64);
;                 y = (lane & 1) ? (other * sn + y * cs) : (y * cs - other * sn);
;             }
;             if (slot < 8) QN[(size_t)(row - NCTX) * 512 + slot * 64 + lane] = f2fp8(y * (0.5f * 1.4426950408889634f));
	v_mul_f32_e32 v11, v28, v11
	v_cndmask_b32_e64 v11, v11, -v11, s[4:5]
	v_fmac_f32_e32 v11, v27, v4
	v_mov_b32_e32 v4, v11
	v_mul_f32_e32 v4, 0x3f38aa3b, v4
	v_mov_b32_e32 v11, 0
	v_cvt_pk_fp8_f32 v11, v4, v4
	global_store_byte v[16:17], v11, off offset:128
	v_mov_b32_e32 v11, 0
	v_mov_b32_e32 v30, 0
	s_waitcnt vmcnt(9)
	v_lshlrev_b32_e32 v4, 16, v113
	v_mul_f32_e32 v31, v4, v4
	s_nop 1
	v_mov_b32_dpp v31, v31 row_shr:1 row_mask:0xf bank_mask:0xf bound_ctrl:1
	v_fmac_f32_e32 v31, v4, v4
	s_nop 1
	v_add_f32_dpp v31, v31, v31 row_shr:2 row_mask:0xf bank_mask:0xf bound_ctrl:1
	s_nop 1
	v_add_f32_dpp v31, v31, v31 row_shr:4 row_mask:0xf bank_mask:0xf bound_ctrl:1
	s_nop 1
	v_add_f32_dpp v31, v31, v31 row_shr:8 row_mask:0xf bank_mask:0xf bound_ctrl:1
	s_nop 1
	v_mov_b32_dpp v11, v31 row_bcast:15 row_mask:0xa bank_mask:0xf bound_ctrl:1
	v_add_f32_e32 v11, v31, v11
	s_nop 1
	v_mov_b32_dpp v30, v11 row_bcast:31 row_mask:0xc bank_mask:0xf bound_ctrl:1
	v_add_f32_e32 v11, v11, v30
	s_nop 0
	v_readlane_b32 s0, v11, 63
	s_nop 1
	v_fma_f32 v11, s0, v24, v3
	v_mul_f32_e32 v30, 0x4b800000, v11
	v_cmp_gt_f32_e64 s[8:9], s24, v11
	s_nop 0
	s_nop 0
	v_cndmask_b32_e64 v11, v11, v30, s[8:9]
	v_rsq_f32_e32 v11, v11
	s_nop 0
	v_mul_f32_e32 v30, 0x45800000, v11
	v_cndmask_b32_e64 v11, v11, v30, s[8:9]
	s_nop 0
	v_mul_f32_e32 v4, v11, v4
	s_nop 0
	v_mov_b32_e32 v11, v22
	v_mul_f32_e32 v4, v11, v4
	v_and_b32_e32 v11, 64, v25
	v_add_u32_e32 v11, 64, v11
	v_cmp_lt_i32_e64 s[8:9], v26, v11
	s_nop 1
	v_cndmask_b32_e64 v11, v25, v26, s[8:9]
	v_lshlrev_b32_e32 v11, 2, v11
	ds_bpermute_b32 v11, v11, v4
	s_waitcnt lgkmcnt(0)
	v_mul_f32_e32 v11, v28, v11
	v_cndmask_b32_e64 v11, v11, -v11, s[4:5]
	v_fmac_f32_e32 v11, v27, v4
	v_mov_b32_e32 v4, v11
	v_mul_f32_e32 v4, 0x3f38aa3b, v4
	v_mov_b32_e32 v11, 0
	v_cvt_pk_fp8_f32 v11, v4, v4
	global_store_byte v[16:17], v11, off offset:192
	v_mov_b32_e32 v11, 0
	v_mov_b32_e32 v30, 0
	s_waitcnt vmcnt(9)
	v_lshlrev_b32_e32 v4, 16, v114
	v_mul_f32_e32 v31, v4, v4
	s_nop 1
	v_mov_b32_dpp v31, v31 row_shr:1 row_mask:0xf bank_mask:0xf bound_ctrl:1
	v_fmac_f32_e32 v31, v4, v4
	s_nop 1
	v_add_f32_dpp v31, v31, v31 row_shr:2 row_mask:0xf bank_mask:0xf bound_ctrl:1
	s_nop 1
	v_add_f32_dpp v31, v31, v31 row_shr:4 row_mask:0xf bank_mask:0xf bound_ctrl:1
	s_nop 1
	v_add_f32_dpp v31, v31, v31 row_shr:8 row_mask:0xf bank_mask:0xf bound_ctrl:1
	s_nop 1
	v_mov_b32_dpp v11, v31 row_bcast:15 row_mask:0xa bank_mask:0xf bound_ctrl:1
	v_add_f32_e32 v11, v31, v11
	s_nop 1
	v_mov_b32_dpp v30, v11 row_bcast:31 row_mask:0xc bank_mask:0xf bound_ctrl:1
	v_add_f32_e32 v11, v11, v30
	s_nop 0
	v_readlane_b32 s0, v11, 63
	s_nop 1
	v_fma_f32 v11, s0, v24, v3
	v_mul_f32_e32 v30, 0x4b800000, v11
	v_cmp_gt_f32_e64 s[8:9], s24, v11
	s_nop 0
	s_nop 0
	v_cndmask_b32_e64 v11, v11, v30, s[8:9]
	v_rsq_f32_e32 v11, v11
	s_nop 0
	v_mul_f32_e32 v30, 0x45800000, v11
	v_cndmask_b32_e64 v11, v11, v30, s[8:9]
	s_nop 0
	v_mul_f32_e32 v4, v11, v4
	s_nop 0
	v_mov_b32_e32 v11, v22
	v_mul_f32_e32 v4, v11, v4
	v_and_b32_e32 v11, 64, v25
	v_add_u32_e32 v11, 64, v11
	v_cmp_lt_i32_e64 s[8:9], v26, v11
	s_nop 1
	v_cndmask_b32_e64 v11, v25, v26, s[8:9]
	v_lshlrev_b32_e32 v11, 2, v11
	ds_bpermute_b32 v11, v11, v4
	s_waitcnt lgkmcnt(0)
	v_mul_f32_e32 v11, v28, v11
	v_cndmask_b32_e64 v11, v11, -v11, s[4:5]
	v_fmac_f32_e32 v11, v27, v4
	v_mov_b32_e32 v4, v11
	v_mul_f32_e32 v4, 0x3f38aa3b, v4
	v_mov_b32_e32 v11, 0
	v_cvt_pk_fp8_f32 v11, v4, v4
	global_store_byte v[16:17], v11, off offset:256
	v_mov_b32_e32 v11, 0
	v_mov_b32_e32 v30, 0
	s_waitcnt vmcnt(9)
	v_lshlrev_b32_e32 v4, 16, v115
	v_mul_f32_e32 v31, v4, v4
	s_nop 1
	v_mov_b32_dpp v31, v31 row_shr:1 row_mask:0xf bank_mask:0xf bound_ctrl:1
	v_fmac_f32_e32 v31, v4, v4
	s_nop 1
	v_add_f32_dpp v31, v31, v31 row_shr:2 row_mask:0xf bank_mask:0xf bound_ctrl:1
	s_nop 1
	v_add_f32_dpp v31, v31, v31 row_shr:4 row_mask:0xf bank_mask:0xf bound_ctrl:1
	s_nop 1
	v_add_f32_dpp v31, v31, v31 row_shr:8 row_mask:0xf bank_mask:0xf bound_ctrl:1
	s_nop 1
	v_mov_b32_dpp v11, v31 row_bcast:15 row_mask:0xa bank_mask:0xf bound_ctrl:1
	v_add_f32_e32 v11, v31, v11
	s_nop 1
	v_mov_b32_dpp v30, v11 row_bcast:31 row_mask:0xc bank_mask:0xf bound_ctrl:1
	v_add_f32_e32 v11, v11, v30
	s_nop 0
	v_readlane_b32 s0, v11, 63
	s_nop 1
	v_fma_f32 v11, s0, v24, v3
	v_mul_f32_e32 v30, 0x4b800000, v11
	v_cmp_gt_f32_e64 s[8:9], s24, v11
	s_nop 0
	s_nop 0
	v_cndmask_b32_e64 v11, v11, v30, s[8:9]
	v_rsq_f32_e32 v11, v11
	s_nop 0
	v_mul_f32_e32 v30, 0x45800000, v11
	v_cndmask_b32_e64 v11, v11, v30, s[8:9]
	s_nop 0
	v_mul_f32_e32 v4, v11, v4
	s_nop 0
	v_mov_b32_e32 v11, v22
	v_mul_f32_e32 v4, v11, v4
	v_and_b32_e32 v11, 64, v25
	v_add_u32_e32 v11, 64, v11
	v_cmp_lt_i32_e64 s[8:9], v26, v11
	s_nop 1
	v_cndmask_b32_e64 v11, v25, v26, s[8:9]
	v_lshlrev_b32_e32 v11, 2, v11
	ds_bpermute_b32 v11, v11, v4
	s_waitcnt lgkmcnt(0)
	v_mul_f32_e32 v11, v28, v11
	v_cndmask_b32_e64 v11, v11, -v11, s[4:5]
	v_fmac_f32_e32 v11, v27, v4
	v_mov_b32_e32 v4, v11
	v_mul_f32_e32 v4, 0x3f38aa3b, v4
	v_mov_b32_e32 v11, 0
	v_cvt_pk_fp8_f32 v11, v4, v4
	global_store_byte v[16:17], v11, off offset:320
	v_mov_b32_e32 v11, 0
	v_mov_b32_e32 v30, 0
	s_waitcnt vmcnt(9)
; __device__ __forceinline__ float bf2f(bfr h) { return __uint_as_float(((unsigned)h) << 16); }
; __device__ __forceinline__ unsigned char f2fp8(float f) { return (unsigned char)(__builtin_amdgcn_cvt_pk_fp8_f32(f, f, 0, false) & 0xff); }
; __device__ __forceinline__ void phase_qkprep_s5a(const Params& P, float* sm, int bid, int nb) {
;     ...
;         for (int slot = lat ? 0 : 8; slot < 10; ++slot) {
;             const float x = bf2f(src[slot * 64]);
;             const float ss = wave_sum(x * x);
;             float y = x * rsqrtf(ss * (1.f / 64.f) + 1e-6f) * (slot < 8 ? qg : kg);
;             if (lat) {
;                 const float other = __shfl_xor(y, 1, 64);
;                 y = (lane & 1) ? (other * sn + y * cs) : (y * cs - other * sn);
;             }
;             if (slot < 8) QN[(size_t)(row - NCTX) * 512 + slot * 64 + lane] = f2fp8(y * (0.5f * 1.4426950408889634f));
;             else KN[(size_t)row * 128 + (slot - 8) * 64 + lane] = f2fp8(y * 0.25f);
;         }
	v_lshlrev_b32_e32 v4, 16, v116
	v_mul_f32_e32 v31, v4, v4
	s_nop 1
	v_mov_b32_dpp v31, v31 row_shr:1 row_mask:0xf bank_mask:0xf bound_ctrl:1
	v_fmac_f32_e32 v31, v4, v4
	s_nop 1
	v_add_f32_dpp v31, v31, v31 row_shr:2 row_mask:0xf bank_mask:0xf bound_ctrl:1
	s_nop 1
	v_add_f32_dpp v31, v31, v31 row_shr:4 row_mask:0xf bank_mask:0xf bound_ctrl:1
	s_nop 1
	v_add_f32_dpp v31, v31, v31 row_shr:8 row_mask:0xf bank_mask:0xf bound_ctrl:1
	s_nop 1
	v_mov_b32_dpp v11, v31 row_bcast:15 row_mask:0xa bank_mask:0xf bound_ctrl:1
	v_add_f32_e32 v11, v31, v11
	s_nop 1
	v_mov_b32_dpp v30, v11 row_bcast:31 row_mask:0xc bank_mask:0xf bound_ctrl:1
	v_add_f32_e32 v11, v11, v30
	s_nop 0
	v_readlane_b32 s0, v11, 63
	s_nop 1
	v_fma_f32 v11, s0, v24, v3
	v_mul_f32_e32 v30, 0x4b800000, v11
	v_cmp_gt_f32_e64 s[8:9], s24, v11
	s_nop 0
	s_nop 0
	v_cndmask_b32_e64 v11, v11, v30, s[8:9]
	v_rsq_f32_e32 v11, v11
	s_nop 0
	v_mul_f32_e32 v30, 0x45800000, v11
	v_cndmask_b32_e64 v11, v11, v30, s[8:9]
	s_nop 0
	v_mul_f32_e32 v4, v11, v4
	s_nop 0
	v_mov_b32_e32 v11, v22
	v_mul_f32_e32 v4, v11, v4
	v_and_b32_e32 v11, 64, v25
	v_add_u32_e32 v11, 64, v11
	v_cmp_lt_i32_e64 s[8:9], v26, v11
	s_nop 1
	v_cndmask_b32_e64 v11, v25, v26, s[8:9]
	v_lshlrev_b32_e32 v11, 2, v11
	ds_bpermute_b32 v11, v11, v4
	s_waitcnt lgkmcnt(0)
	v_mul_f32_e32 v11, v28, v11
	v_cndmask_b32_e64 v11, v11, -v11, s[4:5]
	v_fmac_f32_e32 v11, v27, v4
	v_mov_b32_e32 v4, v11
	v_mul_f32_e32 v4, 0x3f38aa3b, v4
	v_mov_b32_e32 v11, 0
	v_cvt_pk_fp8_f32 v11, v4, v4
	global_store_byte v[16:17], v11, off offset:384
	v_mov_b32_e32 v11, 0
	v_mov_b32_e32 v30, 0
	s_waitcnt vmcnt(9)
	v_lshlrev_b32_e32 v4, 16, v117
	v_mul_f32_e32 v31, v4, v4
	s_nop 1
	v_mov_b32_dpp v31, v31 row_shr:1 row_mask:0xf bank_mask:0xf bound_ctrl:1
	v_fmac_f32_e32 v31, v4, v4
	s_nop 1
	v_add_f32_dpp v31, v31, v31 row_shr:2 row_mask:0xf bank_mask:0xf bound_ctrl:1
	s_nop 1
	v_add_f32_dpp v31, v31, v31 row_shr:4 row_mask:0xf bank_mask:0xf bound_ctrl:1
	s_nop 1
	v_add_f32_dpp v31, v31, v31 row_shr:8 row_mask:0xf bank_mask:0xf bound_ctrl:1
	s_nop 1
	v_mov_b32_dpp v11, v31 row_bcast:15 row_mask:0xa bank_mask:0xf bound_ctrl:1
	v_add_f32_e32 v11, v31, v11
	s_nop 1
	v_mov_b32_dpp v30, v11 row_bcast:31 row_mask:0xc bank_mask:0xf bound_ctrl:1
	v_add_f32_e32 v11, v11, v30
	s_nop 0
	v_readlane_b32 s0, v11, 63
	s_nop 1
	v_fma_f32 v11, s0, v24, v3
	v_mul_f32_e32 v30, 0x4b800000, v11
	v_cmp_gt_f32_e64 s[8:9], s24, v11
	s_nop 0
	s_nop 0
	v_cndmask_b32_e64 v11, v11, v30, s[8:9]
	v_rsq_f32_e32 v11, v11
	s_nop 0
	v_mul_f32_e32 v30, 0x45800000, v11
	v_cndmask_b32_e64 v11, v11, v30, s[8:9]
	s_nop 0
	v_mul_f32_e32 v4, v11, v4
	s_nop 0
	v_mov_b32_e32 v11, v22
	v_mul_f32_e32 v4, v11, v4
	v_and_b32_e32 v11, 64, v25
	v_add_u32_e32 v11, 64, v11
	v_cmp_lt_i32_e64 s[8:9], v26, v11
	s_nop 1
	v_cndmask_b32_e64 v11, v25, v26, s[8:9]
	v_lshlrev_b32_e32 v11, 2, v11
	ds_bpermute_b32 v11, v11, v4
	s_waitcnt lgkmcnt(0)
	v_mul_f32_e32 v11, v28, v11
	v_cndmask_b32_e64 v11, v11, -v11, s[4:5]
	v_fmac_f32_e32 v11, v27, v4
	v_mov_b32_e32 v4, v11
	v_mul_f32_e32 v4, 0x3f38aa3b, v4
	v_mov_b32_e32 v11, 0
	v_cvt_pk_fp8_f32 v11, v4, v4
	global_store_byte v[16:17], v11, off offset:448
	v_mov_b32_e32 v11, 0
	v_mov_b32_e32 v30, 0
	s_waitcnt vmcnt(9)
	v_lshlrev_b32_e32 v4, 16, v118
	v_mul_f32_e32 v31, v4, v4
	s_nop 1
	v_mov_b32_dpp v31, v31 row_shr:1 row_mask:0xf bank_mask:0xf bound_ctrl:1
	v_fmac_f32_e32 v31, v4, v4
	s_nop 1
	v_add_f32_dpp v31, v31, v31 row_shr:2 row_mask:0xf bank_mask:0xf bound_ctrl:1
	s_nop 1
	v_add_f32_dpp v31, v31, v31 row_shr:4 row_mask:0xf bank_mask:0xf bound_ctrl:1
	s_nop 1
	v_add_f32_dpp v31, v31, v31 row_shr:8 row_mask:0xf bank_mask:0xf bound_ctrl:1
	s_nop 1
	v_mov_b32_dpp v11, v31 row_bcast:15 row_mask:0xa bank_mask:0xf bound_ctrl:1
	v_add_f32_e32 v11, v31, v11
	s_nop 1
	v_mov_b32_dpp v30, v11 row_bcast:31 row_mask:0xc bank_mask:0xf bound_ctrl:1
	v_add_f32_e32 v11, v11, v30
	s_nop 0
	v_readlane_b32 s0, v11, 63
	s_nop 1
	v_fma_f32 v11, s0, v24, v3
	v_mul_f32_e32 v30, 0x4b800000, v11
	v_cmp_gt_f32_e64 s[8:9], s24, v11
	s_nop 0
	s_nop 0
	v_cndmask_b32_e64 v11, v11, v30, s[8:9]
	v_rsq_f32_e32 v11, v11
	s_nop 0
	v_mul_f32_e32 v30, 0x45800000, v11
	v_cndmask_b32_e64 v11, v11, v30, s[8:9]
	s_nop 0
	v_mul_f32_e32 v4, v11, v4
	s_nop 0
	v_mov_b32_e32 v11, v21
	v_mul_f32_e32 v4, v11, v4
	v_and_b32_e32 v11, 64, v25
	v_add_u32_e32 v11, 64, v11
	v_cmp_lt_i32_e64 s[8:9], v26, v11
	s_nop 1
	v_cndmask_b32_e64 v11, v25, v26, s[8:9]
	v_lshlrev_b32_e32 v11, 2, v11
	ds_bpermute_b32 v11, v11, v4
	s_waitcnt lgkmcnt(0)
	v_mul_f32_e32 v11, v28, v11
	v_cndmask_b32_e64 v11, v11, -v11, s[4:5]
	v_fmac_f32_e32 v11, v27, v4
	v_mov_b32_e32 v4, v11
	v_mul_f32_e32 v4, 0x3e800000, v4
	v_mov_b32_e32 v11, 0
	v_cvt_pk_fp8_f32 v11, v4, v4
	global_store_byte v[18:19], v11, off offset:512
	v_mov_b32_e32 v11, 0
	v_mov_b32_e32 v30, 0
	s_waitcnt vmcnt(9)
	v_lshlrev_b32_e32 v4, 16, v119
	v_mul_f32_e32 v31, v4, v4
	s_nop 1
	v_mov_b32_dpp v31, v31 row_shr:1 row_mask:0xf bank_mask:0xf bound_ctrl:1
	v_fmac_f32_e32 v31, v4, v4
	s_nop 1
	v_add_f32_dpp v31, v31, v31 row_shr:2 row_mask:0xf bank_mask:0xf bound_ctrl:1
	s_nop 1
	v_add_f32_dpp v31, v31, v31 row_shr:4 row_mask:0xf bank_mask:0xf bound_ctrl:1
	s_nop 1
	v_add_f32_dpp v31, v31, v31 row_shr:8 row_mask:0xf bank_mask:0xf bound_ctrl:1
	s_nop 1
	v_mov_b32_dpp v11, v31 row_bcast:15 row_mask:0xa bank_mask:0xf bound_ctrl:1
	v_add_f32_e32 v11, v31, v11
	s_nop 1
	v_mov_b32_dpp v30, v11 row_bcast:31 row_mask:0xc bank_mask:0xf bound_ctrl:1
	v_add_f32_e32 v11, v11, v30
	s_nop 0
	v_readlane_b32 s0, v11, 63
	s_nop 1
	v_fma_f32 v11, s0, v24, v3
	v_mul_f32_e32 v30, 0x4b800000, v11
	v_cmp_gt_f32_e64 s[8:9], s24, v11
	s_nop 0
	s_nop 0
	v_cndmask_b32_e64 v11, v11, v30, s[8:9]
	v_rsq_f32_e32 v11, v11
	s_nop 0
	v_mul_f32_e32 v30, 0x45800000, v11
	v_cndmask_b32_e64 v11, v11, v30, s[8:9]
	s_nop 0
	v_mul_f32_e32 v4, v11, v4
	s_nop 0
	v_mov_b32_e32 v11, v21
	v_mul_f32_e32 v4, v11, v4
	v_and_b32_e32 v11, 64, v25
	v_add_u32_e32 v11, 64, v11
	v_cmp_lt_i32_e64 s[8:9], v26, v11
	s_nop 1
	v_cndmask_b32_e64 v11, v25, v26, s[8:9]
	v_lshlrev_b32_e32 v11, 2, v11
	ds_bpermute_b32 v11, v11, v4
	s_waitcnt lgkmcnt(0)
	v_mul_f32_e32 v11, v28, v11
	v_cndmask_b32_e64 v11, v11, -v11, s[4:5]
	v_fmac_f32_e32 v11, v27, v4
	v_mov_b32_e32 v4, v11
	v_mul_f32_e32 v4, 0x3e800000, v4
	v_mov_b32_e32 v11, 0
	v_cvt_pk_fp8_f32 v11, v4, v4
	global_store_byte v[18:19], v11, off offset:576
	s_branch .Lqk_rowdone
; __device__ __forceinline__ float bf2f(bfr h) { return __uint_as_float(((unsigned)h) << 16); }
; __device__ __forceinline__ unsigned char f2fp8(float f) { return (unsigned char)(__builtin_amdgcn_cvt_pk_fp8_f32(f, f, 0, false) & 0xff); }
; __device__ __forceinline__ void phase_qkprep_s5a(const Params& P, float* sm, int bid, int nb) {
;     ...
;         for (int slot = lat ? 0 : 8; slot < 10; ++slot) {
;             const float x = bf2f(src[slot * 64]);
;             const float ss = wave_sum(x * x);
;             float y = x * rsqrtf(ss * (1.f / 64.f) + 1e-6f) * (slot < 8 ? qg : kg);
;             if (lat) {
;                 const float other = __shfl_xor(y, 1, 64);
;                 y = (lane & 1) ? (other * sn + y * cs) : (y * cs - other * sn);
;             }
;             if (slot < 8) QN[(size_t)(row - NCTX) * 512 + slot * 64 + lane] = f2fp8(y * (0.5f * 1.4426950408889634f));
;             else KN[(size_t)row * 128 + (slot - 8) * 64 + lane] = f2fp8(y * 0.25f);
;         }
.Lqk_ctxrow:
	global_load_ushort v110, v[14:15], off
	global_load_ushort v111, v[14:15], off offset:128
	v_mov_b32_e32 v11, 0
	v_mov_b32_e32 v30, 0
	s_waitcnt vmcnt(1)
	v_lshlrev_b32_e32 v4, 16, v110
	v_mul_f32_e32 v31, v4, v4
	s_nop 1
	v_mov_b32_dpp v31, v31 row_shr:1 row_mask:0xf bank_mask:0xf bound_ctrl:1
	v_fmac_f32_e32 v31, v4, v4
	s_nop 1
	v_add_f32_dpp v31, v31, v31 row_shr:2 row_mask:0xf bank_mask:0xf bound_ctrl:1
	s_nop 1
	v_add_f32_dpp v31, v31, v31 row_shr:4 row_mask:0xf bank_mask:0xf bound_ctrl:1
	s_nop 1
	v_add_f32_dpp v31, v31, v31 row_shr:8 row_mask:0xf bank_mask:0xf bound_ctrl:1
	s_nop 1
	v_mov_b32_dpp v11, v31 row_bcast:15 row_mask:0xa bank_mask:0xf bound_ctrl:1
	v_add_f32_e32 v11, v31, v11
	s_nop 1
	v_mov_b32_dpp v30, v11 row_bcast:31 row_mask:0xc bank_mask:0xf bound_ctrl:1
	v_add_f32_e32 v11, v11, v30
	s_nop 0
	v_readlane_b32 s0, v11, 63
	s_nop 1
	v_fma_f32 v11, s0, v24, v3
	v_mul_f32_e32 v30, 0x4b800000, v11
	v_cmp_gt_f32_e64 s[8:9], s24, v11
	s_nop 0
	s_nop 0
	v_cndmask_b32_e64 v11, v11, v30, s[8:9]
	v_rsq_f32_e32 v11, v11
	s_nop 0
	v_mul_f32_e32 v30, 0x45800000, v11
	v_cndmask_b32_e64 v11, v11, v30, s[8:9]
	s_nop 0
	v_mul_f32_e32 v4, v11, v4
	s_nop 0
	v_mov_b32_e32 v11, v21
	v_mul_f32_e32 v4, v11, v4
	v_mul_f32_e32 v4, 0x3e800000, v4
	v_mov_b32_e32 v11, 0
	v_cvt_pk_fp8_f32 v11, v4, v4
	global_store_byte v[18:19], v11, off offset:0
	v_mov_b32_e32 v11, 0
	v_mov_b32_e32 v30, 0
	s_waitcnt vmcnt(1)
	v_lshlrev_b32_e32 v4, 16, v111
	v_mul_f32_e32 v31, v4, v4
	s_nop 1
	v_mov_b32_dpp v31, v31 row_shr:1 row_mask:0xf bank_mask:0xf bound_ctrl:1
	v_fmac_f32_e32 v31, v4, v4
	s_nop 1
	v_add_f32_dpp v31, v31, v31 row_shr:2 row_mask:0xf bank_mask:0xf bound_ctrl:1
	s_nop 1
	v_add_f32_dpp v31, v31, v31 row_shr:4 row_mask:0xf bank_mask:0xf bound_ctrl:1
	s_nop 1
	v_add_f32_dpp v31, v31, v31 row_shr:8 row_mask:0xf bank_mask:0xf bound_ctrl:1
	s_nop 1
	v_mov_b32_dpp v11, v31 row_bcast:15 row_mask:0xa bank_mask:0xf bound_ctrl:1
	v_add_f32_e32 v11, v31, v11
	s_nop 1
	v_mov_b32_dpp v30, v11 row_bcast:31 row_mask:0xc bank_mask:0xf bound_ctrl:1
	v_add_f32_e32 v11, v11, v30
	s_nop 0
	v_readlane_b32 s0, v11, 63
	s_nop 1
	v_fma_f32 v11, s0, v24, v3
	v_mul_f32_e32 v30, 0x4b800000, v11
	v_cmp_gt_f32_e64 s[8:9], s24, v11
	s_nop 0
	s_nop 0
	v_cndmask_b32_e64 v11, v11, v30, s[8:9]
	v_rsq_f32_e32 v11, v11
	s_nop 0
	v_mul_f32_e32 v30, 0x45800000, v11
	v_cndmask_b32_e64 v11, v11, v30, s[8:9]
	s_nop 0
	v_mul_f32_e32 v4, v11, v4
	s_nop 0
	v_mov_b32_e32 v11, v21
	v_mul_f32_e32 v4, v11, v4
	v_mul_f32_e32 v4, 0x3e800000, v4
	v_mov_b32_e32 v11, 0
	v_cvt_pk_fp8_f32 v11, v4, v4
	global_store_byte v[18:19], v11, off offset:64
.Lqk_rowdone:
	s_mov_b64 s[20:21], 0
	s_branch .LBB0_1805

; __device__ __forceinline__ float bf2f(bfr h) { return __uint_as_float(((unsigned)h) << 16); }
; __device__ __forceinline__ unsigned char f2fp8(float f) { return (unsigned char)(__builtin_amdgcn_cvt_pk_fp8_f32(f, f, 0, false) & 0xff); }
; __device__ __forceinline__ void phase_qkprep_s5a(const Params& P, float* sm, int bid, int nb) {
;     ...
;         for (int u = bid; u < NT / 64; u += nb) {
;             __syncthreads();
;             for (int e = threadIdx.x; e < 64 * 128; e += NTHR) {
;                 const int r = e >> 7, c = e & 127;
;                 const int pos = ((r >> 2) & 1) * 32 + (r >> 5) * 16 + ((r >> 3) & 3) * 4 + (r & 3);
;                 tile[c * 68 + pos] = f2fp8(bf2f(QK[(size_t)(u * 64 + r) * 1280 + 640 + c]));
;             }
.LBB0_1819:
	v_mad_i64_i32 v[122:123], s[12:13], v6, s8, v[2:3]
	global_load_ushort v130, v[122:123], off offset:1280
	v_add_u32_e32 v6, 4, v6
	v_mad_i64_i32 v[124:125], s[12:13], v6, s8, v[2:3]
	global_load_ushort v131, v[124:125], off offset:1280
	v_add_u32_e32 v6, 4, v6
	v_mad_i64_i32 v[122:123], s[12:13], v6, s8, v[2:3]
	global_load_ushort v132, v[122:123], off offset:1280
	v_add_u32_e32 v6, 4, v6
	v_mad_i64_i32 v[124:125], s[12:13], v6, s8, v[2:3]
	global_load_ushort v133, v[124:125], off offset:1280
	v_add_u32_e32 v6, 4, v6
	v_mad_i64_i32 v[122:123], s[12:13], v6, s8, v[2:3]
	global_load_ushort v134, v[122:123], off offset:1280
	v_add_u32_e32 v6, 4, v6
	v_mad_i64_i32 v[124:125], s[12:13], v6, s8, v[2:3]
	global_load_ushort v135, v[124:125], off offset:1280
	v_add_u32_e32 v6, 4, v6
	v_mad_i64_i32 v[122:123], s[12:13], v6, s8, v[2:3]
	global_load_ushort v136, v[122:123], off offset:1280
	v_add_u32_e32 v6, 4, v6
	v_mad_i64_i32 v[124:125], s[12:13], v6, s8, v[2:3]
	global_load_ushort v137, v[124:125], off offset:1280
	v_add_u32_e32 v6, 4, v6
	v_mad_i64_i32 v[122:123], s[12:13], v6, s8, v[2:3]
	global_load_ushort v138, v[122:123], off offset:1280
	v_add_u32_e32 v6, 4, v6
	v_mad_i64_i32 v[124:125], s[12:13], v6, s8, v[2:3]
	global_load_ushort v139, v[124:125], off offset:1280
	v_add_u32_e32 v6, 4, v6
	v_mad_i64_i32 v[122:123], s[12:13], v6, s8, v[2:3]
	global_load_ushort v140, v[122:123], off offset:1280
	v_add_u32_e32 v6, 4, v6
	v_mad_i64_i32 v[124:125], s[12:13], v6, s8, v[2:3]
	global_load_ushort v141, v[124:125], off offset:1280
	v_add_u32_e32 v6, 4, v6
	v_mad_i64_i32 v[122:123], s[12:13], v6, s8, v[2:3]
	global_load_ushort v142, v[122:123], off offset:1280
	v_add_u32_e32 v6, 4, v6
	v_mad_i64_i32 v[124:125], s[12:13], v6, s8, v[2:3]
	global_load_ushort v143, v[124:125], off offset:1280
	v_add_u32_e32 v6, 4, v6
	v_mad_i64_i32 v[122:123], s[12:13], v6, s8, v[2:3]
	global_load_ushort v144, v[122:123], off offset:1280
	v_add_u32_e32 v6, 4, v6
	v_mad_i64_i32 v[124:125], s[12:13], v6, s8, v[2:3]
	global_load_ushort v145, v[124:125], off offset:1280
	v_add_u32_e32 v6, 4, v6
	v_mov_b32_e32 v21, 0
	v_and_b32_e32 v18, 32, v7
	v_and_b32_e32 v19, 28, v15
	v_add_u32_e32 v18, v9, v18
	v_add_u32_e32 v15, 2, v15
	v_add_u32_e32 v7, 32, v7
	s_waitcnt vmcnt(15)
	v_lshlrev_b32_e32 v17, 16, v130
	v_cvt_pk_fp8_f32 v21, v17, v17
	v_add3_u32 v17, v18, v19, v8
	ds_write_b8 v17, v21 offset:16
	v_mov_b32_e32 v21, 0
	v_and_b32_e32 v18, 32, v7
	v_and_b32_e32 v19, 28, v15
	v_add_u32_e32 v18, v9, v18
	v_add_u32_e32 v15, 2, v15
	v_add_u32_e32 v7, 32, v7
	s_waitcnt vmcnt(14)
	v_lshlrev_b32_e32 v17, 16, v131
	v_cvt_pk_fp8_f32 v21, v17, v17
	v_add3_u32 v17, v18, v19, v8
	ds_write_b8 v17, v21 offset:16
	v_mov_b32_e32 v21, 0
	v_and_b32_e32 v18, 32, v7
	v_and_b32_e32 v19, 28, v15
	v_add_u32_e32 v18, v9, v18
	v_add_u32_e32 v15, 2, v15
	v_add_u32_e32 v7, 32, v7
	s_waitcnt vmcnt(13)
	v_lshlrev_b32_e32 v17, 16, v132
	v_cvt_pk_fp8_f32 v21, v17, v17
	v_add3_u32 v17, v18, v19, v8
	ds_write_b8 v17, v21 offset:16
	v_mov_b32_e32 v21, 0
	v_and_b32_e32 v18, 32, v7
	v_and_b32_e32 v19, 28, v15
	v_add_u32_e32 v18, v9, v18
	v_add_u32_e32 v15, 2, v15
	v_add_u32_e32 v7, 32, v7
	s_waitcnt vmcnt(12)
	v_lshlrev_b32_e32 v17, 16, v133
	v_cvt_pk_fp8_f32 v21, v17, v17
	v_add3_u32 v17, v18, v19, v8
	ds_write_b8 v17, v21 offset:16
	v_mov_b32_e32 v21, 0
	v_and_b32_e32 v18, 32, v7
	v_and_b32_e32 v19, 28, v15
	v_add_u32_e32 v18, v9, v18
	v_add_u32_e32 v15, 2, v15
	v_add_u32_e32 v7, 32, v7
	s_waitcnt vmcnt(11)
; __device__ __forceinline__ float bf2f(bfr h) { return __uint_as_float(((unsigned)h) << 16); }
; __device__ __forceinline__ unsigned char f2fp8(float f) { return (unsigned char)(__builtin_amdgcn_cvt_pk_fp8_f32(f, f, 0, false) & 0xff); }
; __device__ __forceinline__ void phase_qkprep_s5a(const Params& P, float* sm, int bid, int nb) {
;     ...
;         for (int u = bid; u < NT / 64; u += nb) {
;             __syncthreads();
;             for (int e = threadIdx.x; e < 64 * 128; e += NTHR) {
;                 const int r = e >> 7, c = e & 127;
;                 const int pos = ((r >> 2) & 1) * 32 + (r >> 5) * 16 + ((r >> 3) & 3) * 4 + (r & 3);
;                 tile[c * 68 + pos] = f2fp8(bf2f(QK[(size_t)(u * 64 + r) * 1280 + 640 + c]));
;             }
;             __syncthreads();
;             for (int e = threadIdx.x; e < 128 * 16; e += NTHR) { const int c = e >> 4, w = e & 15; *(unsigned*)&VT[(size_t)c * NT + u * 64 + w * 4] = *(const unsigned*)&tile[c * 68 + w * 4]; }
	v_lshlrev_b32_e32 v17, 16, v134
	v_cvt_pk_fp8_f32 v21, v17, v17
	v_add3_u32 v17, v18, v19, v8
	ds_write_b8 v17, v21 offset:16
	v_mov_b32_e32 v21, 0
	v_and_b32_e32 v18, 32, v7
	v_and_b32_e32 v19, 28, v15
	v_add_u32_e32 v18, v9, v18
	v_add_u32_e32 v15, 2, v15
	v_add_u32_e32 v7, 32, v7
	s_waitcnt vmcnt(10)
	v_lshlrev_b32_e32 v17, 16, v135
	v_cvt_pk_fp8_f32 v21, v17, v17
	v_add3_u32 v17, v18, v19, v8
	ds_write_b8 v17, v21 offset:16
	v_mov_b32_e32 v21, 0
	v_and_b32_e32 v18, 32, v7
	v_and_b32_e32 v19, 28, v15
	v_add_u32_e32 v18, v9, v18
	v_add_u32_e32 v15, 2, v15
	v_add_u32_e32 v7, 32, v7
	s_waitcnt vmcnt(9)
	v_lshlrev_b32_e32 v17, 16, v136
	v_cvt_pk_fp8_f32 v21, v17, v17
	v_add3_u32 v17, v18, v19, v8
	ds_write_b8 v17, v21 offset:16
	v_mov_b32_e32 v21, 0
	v_and_b32_e32 v18, 32, v7
	v_and_b32_e32 v19, 28, v15
	v_add_u32_e32 v18, v9, v18
	v_add_u32_e32 v15, 2, v15
	v_add_u32_e32 v7, 32, v7
	s_waitcnt vmcnt(8)
	v_lshlrev_b32_e32 v17, 16, v137
	v_cvt_pk_fp8_f32 v21, v17, v17
	v_add3_u32 v17, v18, v19, v8
	ds_write_b8 v17, v21 offset:16
	v_mov_b32_e32 v21, 0
	v_and_b32_e32 v18, 32, v7
	v_and_b32_e32 v19, 28, v15
	v_add_u32_e32 v18, v9, v18
	v_add_u32_e32 v15, 2, v15
	v_add_u32_e32 v7, 32, v7
	s_waitcnt vmcnt(7)
	v_lshlrev_b32_e32 v17, 16, v138
	v_cvt_pk_fp8_f32 v21, v17, v17
	v_add3_u32 v17, v18, v19, v8
	ds_write_b8 v17, v21 offset:16
	v_mov_b32_e32 v21, 0
	v_and_b32_e32 v18, 32, v7
	v_and_b32_e32 v19, 28, v15
	v_add_u32_e32 v18, v9, v18
	v_add_u32_e32 v15, 2, v15
	v_add_u32_e32 v7, 32, v7
	s_waitcnt vmcnt(6)
	v_lshlrev_b32_e32 v17, 16, v139
	v_cvt_pk_fp8_f32 v21, v17, v17
	v_add3_u32 v17, v18, v19, v8
	ds_write_b8 v17, v21 offset:16
	v_mov_b32_e32 v21, 0
	v_and_b32_e32 v18, 32, v7
	v_and_b32_e32 v19, 28, v15
	v_add_u32_e32 v18, v9, v18
	v_add_u32_e32 v15, 2, v15
	v_add_u32_e32 v7, 32, v7
	s_waitcnt vmcnt(5)
	v_lshlrev_b32_e32 v17, 16, v140
	v_cvt_pk_fp8_f32 v21, v17, v17
	v_add3_u32 v17, v18, v19, v8
	ds_write_b8 v17, v21 offset:16
	v_mov_b32_e32 v21, 0
	v_and_b32_e32 v18, 32, v7
	v_and_b32_e32 v19, 28, v15
	v_add_u32_e32 v18, v9, v18
	v_add_u32_e32 v15, 2, v15
	v_add_u32_e32 v7, 32, v7
	s_waitcnt vmcnt(4)
	v_lshlrev_b32_e32 v17, 16, v141
	v_cvt_pk_fp8_f32 v21, v17, v17
	v_add3_u32 v17, v18, v19, v8
	ds_write_b8 v17, v21 offset:16
	v_mov_b32_e32 v21, 0
	v_and_b32_e32 v18, 32, v7
	v_and_b32_e32 v19, 28, v15
	v_add_u32_e32 v18, v9, v18
	v_add_u32_e32 v15, 2, v15
	v_add_u32_e32 v7, 32, v7
	s_waitcnt vmcnt(3)
	v_lshlrev_b32_e32 v17, 16, v142
	v_cvt_pk_fp8_f32 v21, v17, v17
	v_add3_u32 v17, v18, v19, v8
	ds_write_b8 v17, v21 offset:16
	v_mov_b32_e32 v21, 0
	v_and_b32_e32 v18, 32, v7
	v_and_b32_e32 v19, 28, v15
	v_add_u32_e32 v18, v9, v18
	v_add_u32_e32 v15, 2, v15
	v_add_u32_e32 v7, 32, v7
	s_waitcnt vmcnt(2)
	v_lshlrev_b32_e32 v17, 16, v143
	v_cvt_pk_fp8_f32 v21, v17, v17
	v_add3_u32 v17, v18, v19, v8
	ds_write_b8 v17, v21 offset:16
	v_mov_b32_e32 v21, 0
	v_and_b32_e32 v18, 32, v7
	v_and_b32_e32 v19, 28, v15
	v_add_u32_e32 v18, v9, v18
	v_add_u32_e32 v15, 2, v15
	v_add_u32_e32 v7, 32, v7
	s_waitcnt vmcnt(1)
	v_lshlrev_b32_e32 v17, 16, v144
	v_cvt_pk_fp8_f32 v21, v17, v17
	v_add3_u32 v17, v18, v19, v8
	ds_write_b8 v17, v21 offset:16
	v_mov_b32_e32 v21, 0
	v_and_b32_e32 v18, 32, v7
	v_and_b32_e32 v19, 28, v15
	v_add_u32_e32 v18, v9, v18
	v_add_u32_e32 v15, 2, v15
	v_add_u32_e32 v7, 32, v7
	s_waitcnt vmcnt(0)
	v_lshlrev_b32_e32 v17, 16, v145
	v_cvt_pk_fp8_f32 v21, v17, v17
	v_add3_u32 v17, v18, v19, v8
	ds_write_b8 v17, v21 offset:16
	s_or_b64 exec, exec, s[6:7]
	s_ashr_i32 s1, s0, 31
	v_lshl_add_u64 v[6:7], v[4:5], 0, s[0:1]
	s_mov_b64 s[6:7], 0
	v_mov_b32_e32 v15, v14
	v_mov_b32_e32 v16, v10
	s_waitcnt lgkmcnt(0)
	s_barrier

; __device__ __forceinline__ void phase_s5c(const Params& P, unsigned char* smraw, int bid, int nb) {
;     ...
;     for (int item = bid; item < 256; item += nb) {
;         const int g = item & 31, nt8 = item >> 5;
;         __syncthreads();
;         for (int e = tid; e < 4096; e += NTHR) {
;             const int tl = e >> 6, l = e & 63;
;             const int row = NCTX + (nt8 * 32 + (l & 31)) * 64 + tl;
;             *(u32x4*)&Us[(size_t)e * 8] = *(const u32x4*)(QK + (size_t)row * 1280 + 768 + g * 16 + (l >> 5) * 8);
;         }
;         f32x16 acc[4];
; #pragma unroll
;         for (int m = 0; m < 4; ++m)
; #pragma unroll
;             for (int q = 0; q < 16; ++q) acc[m][q] = 0.f;
; #pragma unroll
;         for (int dir = 0; dir < 2; ++dir) {
;             const int dg = dir * 32 + g;
;             __syncthreads();
;             for (int e = tid; e < 4096; e += NTHR) *(u32x4*)&Fs[(size_t)e * 8] = *(const u32x4*)(S5F + (size_t)dg * 32768 + (size_t)e * 8);
.LBB0_1954:
	v_mov_b64_e32 v[6:7], s[54:55]
	v_and_b32_e32 v8, 8, v3
	v_mad_i64_i32 v[6:7], s[8:9], v2, s27, v[6:7]
	v_lshlrev_b32_e32 v78, 1, v8
	v_lshl_add_u64 v[6:7], v[6:7], 0, s[2:3]
	v_lshl_add_u64 v[6:7], v[6:7], 0, v[78:79]
	v_add_co_u32_e32 v6, vcc, 0x7078000, v6
	s_nop 1
	v_addc_co_u32_e32 v7, vcc, 0, v7, vcc
	global_load_dwordx4 v[124:127], v[6:7], off offset:1536
	v_add_u32_e32 v3, 0x80, v3
	v_add_u32_e32 v2, 8, v2
	v_mov_b64_e32 v[10:11], s[54:55]
	v_and_b32_e32 v8, 8, v3
	v_mad_i64_i32 v[10:11], s[8:9], v2, s27, v[10:11]
	v_lshlrev_b32_e32 v78, 1, v8
	v_lshl_add_u64 v[10:11], v[10:11], 0, s[2:3]
	v_lshl_add_u64 v[10:11], v[10:11], 0, v[78:79]
	v_add_co_u32_e32 v10, vcc, 0x7078000, v10
	s_nop 1
	v_addc_co_u32_e32 v11, vcc, 0, v11, vcc
	global_load_dwordx4 v[128:131], v[10:11], off offset:1536
	v_add_u32_e32 v3, 0x80, v3
	v_add_u32_e32 v2, 8, v2
	v_mov_b64_e32 v[6:7], s[54:55]
	v_and_b32_e32 v8, 8, v3
	v_mad_i64_i32 v[6:7], s[8:9], v2, s27, v[6:7]
	v_lshlrev_b32_e32 v78, 1, v8
	v_lshl_add_u64 v[6:7], v[6:7], 0, s[2:3]
	v_lshl_add_u64 v[6:7], v[6:7], 0, v[78:79]
	v_add_co_u32_e32 v6, vcc, 0x7078000, v6
	s_nop 1
	v_addc_co_u32_e32 v7, vcc, 0, v7, vcc
	global_load_dwordx4 v[132:135], v[6:7], off offset:1536
	v_add_u32_e32 v3, 0x80, v3
	v_add_u32_e32 v2, 8, v2
	v_mov_b64_e32 v[10:11], s[54:55]
	v_and_b32_e32 v8, 8, v3
	v_mad_i64_i32 v[10:11], s[8:9], v2, s27, v[10:11]
	v_lshlrev_b32_e32 v78, 1, v8
	v_lshl_add_u64 v[10:11], v[10:11], 0, s[2:3]
	v_lshl_add_u64 v[10:11], v[10:11], 0, v[78:79]
	v_add_co_u32_e32 v10, vcc, 0x7078000, v10
	s_nop 1
	v_addc_co_u32_e32 v11, vcc, 0, v11, vcc
	global_load_dwordx4 v[136:139], v[10:11], off offset:1536
	v_add_u32_e32 v3, 0x80, v3
	v_add_u32_e32 v2, 8, v2
	v_mov_b64_e32 v[6:7], s[54:55]
	v_and_b32_e32 v8, 8, v3
	v_mad_i64_i32 v[6:7], s[8:9], v2, s27, v[6:7]
	v_lshlrev_b32_e32 v78, 1, v8
	v_lshl_add_u64 v[6:7], v[6:7], 0, s[2:3]
	v_lshl_add_u64 v[6:7], v[6:7], 0, v[78:79]
	v_add_co_u32_e32 v6, vcc, 0x7078000, v6
	s_nop 1
	v_addc_co_u32_e32 v7, vcc, 0, v7, vcc
	global_load_dwordx4 v[140:143], v[6:7], off offset:1536
	v_add_u32_e32 v3, 0x80, v3
	v_add_u32_e32 v2, 8, v2
	v_mov_b64_e32 v[10:11], s[54:55]
	v_and_b32_e32 v8, 8, v3
	v_mad_i64_i32 v[10:11], s[8:9], v2, s27, v[10:11]
	v_lshlrev_b32_e32 v78, 1, v8
	v_lshl_add_u64 v[10:11], v[10:11], 0, s[2:3]
	v_lshl_add_u64 v[10:11], v[10:11], 0, v[78:79]
	v_add_co_u32_e32 v10, vcc, 0x7078000, v10
	s_nop 1
	v_addc_co_u32_e32 v11, vcc, 0, v11, vcc
	global_load_dwordx4 v[144:147], v[10:11], off offset:1536
	v_add_u32_e32 v3, 0x80, v3
	v_add_u32_e32 v2, 8, v2
	v_mov_b64_e32 v[6:7], s[54:55]
	v_and_b32_e32 v8, 8, v3
	v_mad_i64_i32 v[6:7], s[8:9], v2, s27, v[6:7]
	v_lshlrev_b32_e32 v78, 1, v8
	v_lshl_add_u64 v[6:7], v[6:7], 0, s[2:3]
	v_lshl_add_u64 v[6:7], v[6:7], 0, v[78:79]
	v_add_co_u32_e32 v6, vcc, 0x7078000, v6
	s_nop 1
	v_addc_co_u32_e32 v7, vcc, 0, v7, vcc
	global_load_dwordx4 v[148:151], v[6:7], off offset:1536
	v_add_u32_e32 v3, 0x80, v3
	v_add_u32_e32 v2, 8, v2
	v_mov_b64_e32 v[10:11], s[54:55]
	v_and_b32_e32 v8, 8, v3
	v_mad_i64_i32 v[10:11], s[8:9], v2, s27, v[10:11]
	v_lshlrev_b32_e32 v78, 1, v8
	v_lshl_add_u64 v[10:11], v[10:11], 0, s[2:3]
	v_lshl_add_u64 v[10:11], v[10:11], 0, v[78:79]
	v_add_co_u32_e32 v10, vcc, 0x7078000, v10
	s_nop 1
	v_addc_co_u32_e32 v11, vcc, 0, v11, vcc
	global_load_dwordx4 v[152:155], v[10:11], off offset:1536
	v_add_u32_e32 v3, 0x80, v3
	v_add_u32_e32 v2, 8, v2
	s_waitcnt vmcnt(7)
	ds_write_b128 v4, v[124:127]
	s_waitcnt vmcnt(6)
	ds_write_b128 v4, v[128:131] offset:8192
	s_waitcnt vmcnt(5)
	ds_write_b128 v4, v[132:135] offset:16384
	s_waitcnt vmcnt(4)
	ds_write_b128 v4, v[136:139] offset:24576
	s_waitcnt vmcnt(3)
	ds_write_b128 v4, v[140:143] offset:32768
	s_waitcnt vmcnt(2)
	ds_write_b128 v4, v[144:147] offset:40960
	s_waitcnt vmcnt(1)
	ds_write_b128 v4, v[148:151] offset:49152
	s_waitcnt vmcnt(0)
	ds_write_b128 v4, v[152:155] offset:57344
	s_or_b64 exec, exec, s[0:1]
	s_lshl_b32 s50, s6, 16
	s_add_u32 s0, s20, s50
	s_addc_u32 s1, s21, 0
	v_lshlrev_b32_e32 v78, 1, v74
	v_lshl_add_u64 v[2:3], s[0:1], 0, v[78:79]
	v_add_co_u32_e32 v8, vcc, s25, v2
	s_waitcnt lgkmcnt(0)
	s_nop 0
	v_addc_co_u32_e32 v9, vcc, 0, v3, vcc
	v_add_co_u32_e32 v16, vcc, 0x6000, v2
	s_barrier
	s_nop 0
	v_addc_co_u32_e32 v17, vcc, 0, v3, vcc
	v_add_co_u32_e32 v24, vcc, 0xa000, v2
	s_nop 1
	v_addc_co_u32_e32 v25, vcc, 0, v3, vcc
	global_load_dwordx4 v[4:7], v78, s[0:1]
	s_nop 0
	global_load_dwordx4 v[8:11], v[8:9], off
	s_nop 0
	global_load_dwordx4 v[12:15], v120, s[0:1]
	s_nop 0
	global_load_dwordx4 v[16:19], v[16:17], off
	s_nop 0
	global_load_dwordx4 v[20:23], v121, s[0:1]
	s_nop 0
	global_load_dwordx4 v[24:27], v[24:25], off
	s_nop 0
	global_load_dwordx4 v[28:31], v122, s[0:1]
	s_waitcnt vmcnt(6)
	ds_write_b128 v102, v[4:7]
	s_waitcnt vmcnt(5)
	ds_write_b128 v103, v[8:11]
	s_waitcnt vmcnt(4)
	ds_write_b128 v104, v[12:15]
	s_waitcnt vmcnt(3)
	ds_write_b128 v105, v[16:19]
	s_waitcnt vmcnt(2)
	ds_write_b128 v106, v[20:23]
	s_waitcnt vmcnt(1)
	ds_write_b128 v107, v[24:27]
	s_waitcnt vmcnt(0)
	ds_write_b128 v108, v[28:31]
	s_and_saveexec_b64 s[0:1], s[4:5]
	s_cbranch_execz .LBB0_1957
	v_add_co_u32_e32 v2, vcc, 0xe000, v2
	s_nop 1
	v_addc_co_u32_e32 v3, vcc, 0, v3, vcc
	global_load_dwordx4 v[2:5], v[2:3], off
	s_waitcnt vmcnt(0)
	ds_write_b128 v109, v[2:5]
